# all int8/fp16 GEMM k-loops except the merge GEMM: LDS-DMA stage loads in saddr form (SGPR base + 32-bit lane offset), 16 vector 64-bit address adds per iteration removed
# baseline (speedup 1.0000x reference)
.LBB0_418:
	ds_read_b128 v[148:151], v168
	ds_read_b128 v[152:155], v168 offset:1024
	ds_read_b128 v[172:175], v168 offset:2048
	ds_read_b128 v[176:179], v168 offset:3072
	ds_read_b128 v[186:189], v169
	ds_read_b128 v[190:193], v169 offset:1024
	ds_read_b128 v[194:197], v169 offset:2048
	ds_read_b128 v[198:201], v169 offset:3072
	s_add_u32 s38, s34, 0xfff00080
	s_addc_u32 s39, s35, -1
	s_cmp_eq_u32 s67, 60
	s_cselect_b32 s45, s5, s39
	s_cselect_b32 s44, s7, s38
	s_cselect_b32 s43, s15, s66
	s_cselect_b32 s42, s25, s63
	s_add_i32 m0, s46, 0xc000
	ds_read_b128 v[202:205], v170
	ds_read_b128 v[206:209], v170 offset:1024
	ds_read_b128 v[210:213], v170 offset:2048
	ds_read_b128 v[214:217], v170 offset:3072
	ds_read_b128 v[218:221], v170 offset:4096
	ds_read_b128 v[222:225], v170 offset:5120
	ds_read_b128 v[226:229], v170 offset:6144
	ds_read_b128 v[230:233], v170 offset:7168
	global_load_lds_dwordx4 v140, s[34:35]
	s_add_i32 m0, s46, 0xe000
	s_nop 0
	global_load_lds_dwordx4 v142, s[34:35]
	s_waitcnt vmcnt(8)
	s_waitcnt lgkmcnt(0)
	s_barrier
	s_setprio 1
	s_waitcnt lgkmcnt(0)
	v_mfma_f32_16x16x32_f16 v[126:129], v[148:151], v[202:205], v[126:129]
	v_mfma_f32_16x16x32_f16 v[122:125], v[172:175], v[202:205], v[122:125]
	v_mfma_f32_16x16x32_f16 v[110:113], v[148:151], v[210:213], v[110:113]
	v_mfma_f32_16x16x32_f16 v[106:109], v[172:175], v[210:213], v[106:109]
	v_mfma_f32_16x16x32_f16 v[94:97], v[148:151], v[218:221], v[94:97]
	v_mfma_f32_16x16x32_f16 v[90:93], v[172:175], v[218:221], v[90:93]
	v_mfma_f32_16x16x32_f16 v[78:81], v[148:151], v[226:229], v[78:81]
	v_mfma_f32_16x16x32_f16 v[74:77], v[172:175], v[226:229], v[74:77]
	v_mfma_f32_16x16x32_f16 v[126:129], v[152:155], v[206:209], v[126:129]
	v_mfma_f32_16x16x32_f16 v[122:125], v[176:179], v[206:209], v[122:125]
	v_mfma_f32_16x16x32_f16 v[110:113], v[152:155], v[214:217], v[110:113]
	v_mfma_f32_16x16x32_f16 v[106:109], v[176:179], v[214:217], v[106:109]
	v_mfma_f32_16x16x32_f16 v[94:97], v[152:155], v[222:225], v[94:97]
	v_mfma_f32_16x16x32_f16 v[90:93], v[176:179], v[222:225], v[90:93]
	v_mfma_f32_16x16x32_f16 v[78:81], v[152:155], v[230:233], v[78:81]
	v_mfma_f32_16x16x32_f16 v[74:77], v[176:179], v[230:233], v[74:77]
	s_setprio 0
	s_setprio 1
	v_mfma_f32_16x16x32_f16 v[118:121], v[186:189], v[202:205], v[118:121]
	v_mfma_f32_16x16x32_f16 v[114:117], v[194:197], v[202:205], v[114:117]
	v_mfma_f32_16x16x32_f16 v[102:105], v[186:189], v[210:213], v[102:105]
	v_mfma_f32_16x16x32_f16 v[98:101], v[194:197], v[210:213], v[98:101]
	v_mfma_f32_16x16x32_f16 v[86:89], v[186:189], v[218:221], v[86:89]
	v_mfma_f32_16x16x32_f16 v[82:85], v[194:197], v[218:221], v[82:85]
	v_mfma_f32_16x16x32_f16 v[70:73], v[186:189], v[226:229], v[70:73]
	v_mfma_f32_16x16x32_f16 v[66:69], v[194:197], v[226:229], v[66:69]
	v_mfma_f32_16x16x32_f16 v[118:121], v[190:193], v[206:209], v[118:121]
	v_mfma_f32_16x16x32_f16 v[114:117], v[198:201], v[206:209], v[114:117]
	v_mfma_f32_16x16x32_f16 v[102:105], v[190:193], v[214:217], v[102:105]
	v_mfma_f32_16x16x32_f16 v[98:101], v[198:201], v[214:217], v[98:101]
	v_mfma_f32_16x16x32_f16 v[86:89], v[190:193], v[222:225], v[86:89]
	v_mfma_f32_16x16x32_f16 v[82:85], v[198:201], v[222:225], v[82:85]
	v_mfma_f32_16x16x32_f16 v[70:73], v[190:193], v[230:233], v[70:73]
	v_mfma_f32_16x16x32_f16 v[66:69], v[198:201], v[230:233], v[66:69]
	s_setprio 0
	s_barrier
	s_add_u32 s98, s42, s10
	s_addc_u32 s99, s43, s11
	s_add_u32 s100, s44, s10
	s_addc_u32 s101, s45, s11
	s_add_i32 s38, s61, s33
	s_mov_b32 m0, s38
	ds_read_b128 v[202:205], v170 offset:16384
	ds_read_b128 v[206:209], v170 offset:17408
	ds_read_b128 v[210:213], v170 offset:18432
	ds_read_b128 v[214:217], v170 offset:19456
	ds_read_b128 v[218:221], v170 offset:20480
	ds_read_b128 v[222:225], v170 offset:21504
	ds_read_b128 v[226:229], v170 offset:22528
	ds_read_b128 v[230:233], v170 offset:23552
	global_load_lds_dwordx4 v132, s[42:43]
	s_add_i32 m0, s38, 0x2000
	s_add_u32 s72, s42, 0x100000
	s_addc_u32 s73, s43, 0
	s_add_i32 s38, s62, s33
	global_load_lds_dwordx4 v136, s[42:43]
	s_mov_b32 m0, s38
	s_nop 0
	global_load_lds_dwordx4 v132, s[72:73]
	s_add_i32 m0, s38, 0x2000
	s_nop 0
	global_load_lds_dwordx4 v136, s[72:73]
	s_mov_b32 m0, s46
	s_nop 0
	global_load_lds_dwordx4 v130, s[44:45]
	s_mov_b32 m0, s47
	s_nop 0
	global_load_lds_dwordx4 v134, s[44:45]
	s_waitcnt vmcnt(8)
	s_waitcnt lgkmcnt(0)
	s_barrier
	s_setprio 1
	s_waitcnt lgkmcnt(0)
	v_mfma_f32_16x16x32_f16 v[62:65], v[148:151], v[202:205], v[62:65]
	v_mfma_f32_16x16x32_f16 v[58:61], v[172:175], v[202:205], v[58:61]
	v_mfma_f32_16x16x32_f16 v[46:49], v[148:151], v[210:213], v[46:49]
	v_mfma_f32_16x16x32_f16 v[42:45], v[172:175], v[210:213], v[42:45]
	v_mfma_f32_16x16x32_f16 v[30:33], v[148:151], v[218:221], v[30:33]
	v_mfma_f32_16x16x32_f16 v[26:29], v[172:175], v[218:221], v[26:29]
	v_mfma_f32_16x16x32_f16 v[14:17], v[148:151], v[226:229], v[14:17]
	v_mfma_f32_16x16x32_f16 v[10:13], v[172:175], v[226:229], v[10:13]
	v_mfma_f32_16x16x32_f16 v[62:65], v[152:155], v[206:209], v[62:65]
	v_mfma_f32_16x16x32_f16 v[58:61], v[176:179], v[206:209], v[58:61]
	v_mfma_f32_16x16x32_f16 v[46:49], v[152:155], v[214:217], v[46:49]
	v_mfma_f32_16x16x32_f16 v[42:45], v[176:179], v[214:217], v[42:45]
	v_mfma_f32_16x16x32_f16 v[30:33], v[152:155], v[222:225], v[30:33]
	v_mfma_f32_16x16x32_f16 v[26:29], v[176:179], v[222:225], v[26:29]
	v_mfma_f32_16x16x32_f16 v[14:17], v[152:155], v[230:233], v[14:17]
	v_mfma_f32_16x16x32_f16 v[10:13], v[176:179], v[230:233], v[10:13]
	s_setprio 0
	s_setprio 1
	v_mfma_f32_16x16x32_f16 v[54:57], v[186:189], v[202:205], v[54:57]
	v_mfma_f32_16x16x32_f16 v[50:53], v[194:197], v[202:205], v[50:53]
	v_mfma_f32_16x16x32_f16 v[38:41], v[186:189], v[210:213], v[38:41]
	v_mfma_f32_16x16x32_f16 v[34:37], v[194:197], v[210:213], v[34:37]
	v_mfma_f32_16x16x32_f16 v[22:25], v[186:189], v[218:221], v[22:25]
	v_mfma_f32_16x16x32_f16 v[18:21], v[194:197], v[218:221], v[18:21]
	v_mfma_f32_16x16x32_f16 v[6:9], v[186:189], v[226:229], v[6:9]
	v_mfma_f32_16x16x32_f16 v[2:5], v[194:197], v[226:229], v[2:5]
	v_mfma_f32_16x16x32_f16 v[54:57], v[190:193], v[206:209], v[54:57]
	v_mfma_f32_16x16x32_f16 v[50:53], v[198:201], v[206:209], v[50:53]
	v_mfma_f32_16x16x32_f16 v[38:41], v[190:193], v[214:217], v[38:41]
	v_mfma_f32_16x16x32_f16 v[34:37], v[198:201], v[214:217], v[34:37]
	v_mfma_f32_16x16x32_f16 v[22:25], v[190:193], v[222:225], v[22:25]
	v_mfma_f32_16x16x32_f16 v[18:21], v[198:201], v[222:225], v[18:21]
	v_mfma_f32_16x16x32_f16 v[6:9], v[190:193], v[230:233], v[6:9]
	v_mfma_f32_16x16x32_f16 v[2:5], v[198:201], v[230:233], v[2:5]
	s_setprio 0
	s_barrier
	s_add_i32 s38, 0, 0x18000
	v_add_u32_e32 v138, s38, v164
	s_add_i32 s39, 0, 0x1c000
	ds_read_b128 v[148:151], v138
	ds_read_b128 v[152:155], v138 offset:1024
	ds_read_b128 v[172:175], v138 offset:2048
	ds_read_b128 v[176:179], v138 offset:3072
	v_add_u32_e32 v138, s39, v164
	ds_read_b128 v[186:189], v138
	ds_read_b128 v[190:193], v138 offset:1024
	ds_read_b128 v[194:197], v138 offset:2048
	ds_read_b128 v[198:201], v138 offset:3072
	s_add_u32 s44, s44, 0x100000
	s_addc_u32 s45, s45, 0
	s_mov_b32 m0, s50
	ds_read_b128 v[202:205], v170 offset:32768
	ds_read_b128 v[206:209], v170 offset:33792
	ds_read_b128 v[210:213], v170 offset:34816
	ds_read_b128 v[214:217], v170 offset:35840
	ds_read_b128 v[218:221], v170 offset:36864
	ds_read_b128 v[222:225], v170 offset:37888
	ds_read_b128 v[226:229], v170 offset:38912
	ds_read_b128 v[230:233], v170 offset:39936
	global_load_lds_dwordx4 v130, s[44:45]
	s_mov_b32 m0, s51
	s_nop 0
	global_load_lds_dwordx4 v134, s[44:45]
	s_waitcnt vmcnt(8)
	s_waitcnt lgkmcnt(0)
	s_barrier
	s_setprio 1
	s_waitcnt lgkmcnt(0)
	v_mfma_f32_16x16x32_f16 v[126:129], v[148:151], v[202:205], v[126:129]
	v_mfma_f32_16x16x32_f16 v[122:125], v[172:175], v[202:205], v[122:125]
	v_mfma_f32_16x16x32_f16 v[110:113], v[148:151], v[210:213], v[110:113]
	v_mfma_f32_16x16x32_f16 v[106:109], v[172:175], v[210:213], v[106:109]
	v_mfma_f32_16x16x32_f16 v[94:97], v[148:151], v[218:221], v[94:97]
	v_mfma_f32_16x16x32_f16 v[90:93], v[172:175], v[218:221], v[90:93]
	v_mfma_f32_16x16x32_f16 v[78:81], v[148:151], v[226:229], v[78:81]
	v_mfma_f32_16x16x32_f16 v[74:77], v[172:175], v[226:229], v[74:77]
	v_mfma_f32_16x16x32_f16 v[126:129], v[152:155], v[206:209], v[126:129]
	v_mfma_f32_16x16x32_f16 v[122:125], v[176:179], v[206:209], v[122:125]
	v_mfma_f32_16x16x32_f16 v[110:113], v[152:155], v[214:217], v[110:113]
	v_mfma_f32_16x16x32_f16 v[106:109], v[176:179], v[214:217], v[106:109]
	v_mfma_f32_16x16x32_f16 v[94:97], v[152:155], v[222:225], v[94:97]
	v_mfma_f32_16x16x32_f16 v[90:93], v[176:179], v[222:225], v[90:93]
	v_mfma_f32_16x16x32_f16 v[78:81], v[152:155], v[230:233], v[78:81]
	v_mfma_f32_16x16x32_f16 v[74:77], v[176:179], v[230:233], v[74:77]
	s_setprio 0
	s_setprio 1
	v_mfma_f32_16x16x32_f16 v[118:121], v[186:189], v[202:205], v[118:121]
	v_mfma_f32_16x16x32_f16 v[114:117], v[194:197], v[202:205], v[114:117]
	v_mfma_f32_16x16x32_f16 v[102:105], v[186:189], v[210:213], v[102:105]
	v_mfma_f32_16x16x32_f16 v[98:101], v[194:197], v[210:213], v[98:101]
	v_mfma_f32_16x16x32_f16 v[86:89], v[186:189], v[218:221], v[86:89]
	v_mfma_f32_16x16x32_f16 v[82:85], v[194:197], v[218:221], v[82:85]
	v_mfma_f32_16x16x32_f16 v[70:73], v[186:189], v[226:229], v[70:73]
	v_mfma_f32_16x16x32_f16 v[66:69], v[194:197], v[226:229], v[66:69]
	v_mfma_f32_16x16x32_f16 v[118:121], v[190:193], v[206:209], v[118:121]
	v_mfma_f32_16x16x32_f16 v[114:117], v[198:201], v[206:209], v[114:117]
	v_mfma_f32_16x16x32_f16 v[102:105], v[190:193], v[214:217], v[102:105]
	v_mfma_f32_16x16x32_f16 v[98:101], v[198:201], v[214:217], v[98:101]
	v_mfma_f32_16x16x32_f16 v[86:89], v[190:193], v[222:225], v[86:89]
	v_mfma_f32_16x16x32_f16 v[82:85], v[198:201], v[222:225], v[82:85]
	v_mfma_f32_16x16x32_f16 v[70:73], v[190:193], v[230:233], v[70:73]
	v_mfma_f32_16x16x32_f16 v[66:69], v[198:201], v[230:233], v[66:69]
	s_setprio 0
	s_barrier
	s_add_i32 s38, s38, s33
	s_mov_b32 m0, s38
	ds_read_b128 v[202:205], v170 offset:49152
	ds_read_b128 v[206:209], v170 offset:50176
	ds_read_b128 v[210:213], v170 offset:51200
	ds_read_b128 v[214:217], v170 offset:52224
	ds_read_b128 v[218:221], v170 offset:53248
	ds_read_b128 v[222:225], v170 offset:54272
	ds_read_b128 v[226:229], v170 offset:55296
	ds_read_b128 v[230:233], v170 offset:56320
	global_load_lds_dwordx4 v132, s[98:99]
	s_add_i32 m0, s38, 0x2000
	s_add_u32 s42, s42, 0x100080
	s_addc_u32 s43, s43, 0
	s_add_i32 s38, s39, s33
	global_load_lds_dwordx4 v136, s[98:99]
	s_mov_b32 m0, s38
	s_nop 0
	global_load_lds_dwordx4 v132, s[42:43]
	s_add_i32 m0, s38, 0x2000
	s_nop 0
	global_load_lds_dwordx4 v136, s[42:43]
	s_mov_b32 m0, s53
	s_nop 0
	global_load_lds_dwordx4 v130, s[100:101]
	s_mov_b32 m0, s58
	s_nop 0
	global_load_lds_dwordx4 v134, s[100:101]
	s_waitcnt vmcnt(8)
	s_waitcnt lgkmcnt(0)
	s_barrier
	s_setprio 1
	s_waitcnt lgkmcnt(0)
	v_mfma_f32_16x16x32_f16 v[62:65], v[148:151], v[202:205], v[62:65]
	v_mfma_f32_16x16x32_f16 v[58:61], v[172:175], v[202:205], v[58:61]
	v_mfma_f32_16x16x32_f16 v[46:49], v[148:151], v[210:213], v[46:49]
	v_mfma_f32_16x16x32_f16 v[42:45], v[172:175], v[210:213], v[42:45]
	v_mfma_f32_16x16x32_f16 v[30:33], v[148:151], v[218:221], v[30:33]
	v_mfma_f32_16x16x32_f16 v[26:29], v[172:175], v[218:221], v[26:29]
	v_mfma_f32_16x16x32_f16 v[14:17], v[148:151], v[226:229], v[14:17]
	v_mfma_f32_16x16x32_f16 v[10:13], v[172:175], v[226:229], v[10:13]
	v_mfma_f32_16x16x32_f16 v[62:65], v[152:155], v[206:209], v[62:65]
	v_mfma_f32_16x16x32_f16 v[58:61], v[176:179], v[206:209], v[58:61]
	v_mfma_f32_16x16x32_f16 v[46:49], v[152:155], v[214:217], v[46:49]
	v_mfma_f32_16x16x32_f16 v[42:45], v[176:179], v[214:217], v[42:45]
	v_mfma_f32_16x16x32_f16 v[30:33], v[152:155], v[222:225], v[30:33]
	v_mfma_f32_16x16x32_f16 v[26:29], v[176:179], v[222:225], v[26:29]
	v_mfma_f32_16x16x32_f16 v[14:17], v[152:155], v[230:233], v[14:17]
	v_mfma_f32_16x16x32_f16 v[10:13], v[176:179], v[230:233], v[10:13]
	s_setprio 0
	s_setprio 1
	v_mfma_f32_16x16x32_f16 v[54:57], v[186:189], v[202:205], v[54:57]
	v_mfma_f32_16x16x32_f16 v[50:53], v[194:197], v[202:205], v[50:53]
	v_mfma_f32_16x16x32_f16 v[38:41], v[186:189], v[210:213], v[38:41]
	v_mfma_f32_16x16x32_f16 v[34:37], v[194:197], v[210:213], v[34:37]
	v_mfma_f32_16x16x32_f16 v[22:25], v[186:189], v[218:221], v[22:25]
	v_mfma_f32_16x16x32_f16 v[18:21], v[194:197], v[218:221], v[18:21]
	v_mfma_f32_16x16x32_f16 v[6:9], v[186:189], v[226:229], v[6:9]
	v_mfma_f32_16x16x32_f16 v[2:5], v[194:197], v[226:229], v[2:5]
	v_mfma_f32_16x16x32_f16 v[54:57], v[190:193], v[206:209], v[54:57]
	v_mfma_f32_16x16x32_f16 v[50:53], v[198:201], v[206:209], v[50:53]
	v_mfma_f32_16x16x32_f16 v[38:41], v[190:193], v[214:217], v[38:41]
	v_mfma_f32_16x16x32_f16 v[34:37], v[198:201], v[214:217], v[34:37]
	v_mfma_f32_16x16x32_f16 v[22:25], v[190:193], v[222:225], v[22:25]
	v_mfma_f32_16x16x32_f16 v[18:21], v[198:201], v[222:225], v[18:21]
	v_mfma_f32_16x16x32_f16 v[6:9], v[190:193], v[230:233], v[6:9]
	v_mfma_f32_16x16x32_f16 v[2:5], v[198:201], v[230:233], v[2:5]
	s_setprio 0
	s_barrier
	s_add_i32 s67, s67, 2
	s_add_u32 s34, s34, 0x100
	s_addc_u32 s35, s35, 0
	s_add_u32 s63, s63, 0x100
	s_addc_u32 s66, s66, 0
	s_cmp_gt_u32 s67, 61
	s_cbranch_scc0 .LBB0_418
	s_and_b64 vcc, exec, s[12:13]
	s_cbranch_vccz .LBB0_421
	s_barrier

.LBB0_547:
	ds_read_b128 v[26:29], v191
	ds_read_b128 v[30:33], v191 offset:1024
	ds_read_b128 v[42:45], v191 offset:2048
	ds_read_b128 v[46:49], v191 offset:3072
	ds_read_b128 v[168:171], v192
	ds_read_b128 v[172:175], v192 offset:1024
	ds_read_b128 v[176:179], v192 offset:2048
	ds_read_b128 v[194:197], v192 offset:3072
	s_add_u32 s38, s34, 0xfff80080
	s_addc_u32 s39, s35, -1
	s_cmp_eq_u32 s74, 28
	s_cselect_b32 s45, s5, s39
	s_cselect_b32 s44, s7, s38
	s_cselect_b32 s43, s8, s73
	s_cselect_b32 s42, s65, s67
	s_add_i32 m0, s50, 0xc000
	ds_read_b128 v[198:201], v193
	ds_read_b128 v[202:205], v193 offset:1024
	ds_read_b128 v[206:209], v193 offset:2048
	ds_read_b128 v[210:213], v193 offset:3072
	ds_read_b128 v[214:217], v193 offset:4096
	ds_read_b128 v[218:221], v193 offset:5120
	ds_read_b128 v[222:225], v193 offset:6144
	ds_read_b128 v[226:229], v193 offset:7168
	global_load_lds_dwordx4 v156, s[34:35]
	s_add_i32 m0, s50, 0xe000
	s_nop 0
	global_load_lds_dwordx4 v158, s[34:35]
	s_waitcnt vmcnt(8)
	s_waitcnt lgkmcnt(0)
	s_barrier
	s_setprio 1
	s_waitcnt lgkmcnt(0)
	v_mfma_i32_16x16x64_i8 v[142:145], v[26:29], v[198:201], v[142:145]
	v_mfma_i32_16x16x64_i8 v[138:141], v[42:45], v[198:201], v[138:141]
	v_mfma_i32_16x16x64_i8 v[126:129], v[26:29], v[206:209], v[126:129]
	v_mfma_i32_16x16x64_i8 v[122:125], v[42:45], v[206:209], v[122:125]
	v_mfma_i32_16x16x64_i8 v[110:113], v[26:29], v[214:217], v[110:113]
	v_mfma_i32_16x16x64_i8 v[106:109], v[42:45], v[214:217], v[106:109]
	v_mfma_i32_16x16x64_i8 v[94:97], v[26:29], v[222:225], v[94:97]
	v_mfma_i32_16x16x64_i8 v[90:93], v[42:45], v[222:225], v[90:93]
	v_mfma_i32_16x16x64_i8 v[142:145], v[30:33], v[202:205], v[142:145]
	v_mfma_i32_16x16x64_i8 v[138:141], v[46:49], v[202:205], v[138:141]
	v_mfma_i32_16x16x64_i8 v[126:129], v[30:33], v[210:213], v[126:129]
	v_mfma_i32_16x16x64_i8 v[122:125], v[46:49], v[210:213], v[122:125]
	v_mfma_i32_16x16x64_i8 v[110:113], v[30:33], v[218:221], v[110:113]
	v_mfma_i32_16x16x64_i8 v[106:109], v[46:49], v[218:221], v[106:109]
	v_mfma_i32_16x16x64_i8 v[94:97], v[30:33], v[226:229], v[94:97]
	v_mfma_i32_16x16x64_i8 v[90:93], v[46:49], v[226:229], v[90:93]
	s_setprio 0
	s_setprio 1
	v_mfma_i32_16x16x64_i8 v[134:137], v[168:171], v[198:201], v[134:137]
	v_mfma_i32_16x16x64_i8 v[130:133], v[176:179], v[198:201], v[130:133]
	v_mfma_i32_16x16x64_i8 v[118:121], v[168:171], v[206:209], v[118:121]
	v_mfma_i32_16x16x64_i8 v[114:117], v[176:179], v[206:209], v[114:117]
	v_mfma_i32_16x16x64_i8 v[102:105], v[168:171], v[214:217], v[102:105]
	v_mfma_i32_16x16x64_i8 v[98:101], v[176:179], v[214:217], v[98:101]
	v_mfma_i32_16x16x64_i8 v[86:89], v[168:171], v[222:225], v[86:89]
	v_mfma_i32_16x16x64_i8 v[82:85], v[176:179], v[222:225], v[82:85]
	v_mfma_i32_16x16x64_i8 v[134:137], v[172:175], v[202:205], v[134:137]
	v_mfma_i32_16x16x64_i8 v[130:133], v[194:197], v[202:205], v[130:133]
	v_mfma_i32_16x16x64_i8 v[118:121], v[172:175], v[210:213], v[118:121]
	v_mfma_i32_16x16x64_i8 v[114:117], v[194:197], v[210:213], v[114:117]
	v_mfma_i32_16x16x64_i8 v[102:105], v[172:175], v[218:221], v[102:105]
	v_mfma_i32_16x16x64_i8 v[98:101], v[194:197], v[218:221], v[98:101]
	v_mfma_i32_16x16x64_i8 v[86:89], v[172:175], v[226:229], v[86:89]
	v_mfma_i32_16x16x64_i8 v[82:85], v[194:197], v[226:229], v[82:85]
	s_setprio 0
	s_barrier
	s_add_u32 s98, s42, s12
	s_addc_u32 s99, s43, s13
	s_add_u32 s100, s44, s12
	s_addc_u32 s101, s45, s13
	s_add_i32 s38, s62, s47
	s_mov_b32 m0, s38
	ds_read_b128 v[198:201], v193 offset:16384
	ds_read_b128 v[202:205], v193 offset:17408
	ds_read_b128 v[206:209], v193 offset:18432
	ds_read_b128 v[210:213], v193 offset:19456
	ds_read_b128 v[214:217], v193 offset:20480
	ds_read_b128 v[218:221], v193 offset:21504
	ds_read_b128 v[222:225], v193 offset:22528
	ds_read_b128 v[226:229], v193 offset:23552
	global_load_lds_dwordx4 v148, s[42:43]
	s_add_i32 m0, s38, 0x2000
	s_add_u32 s76, s42, 0x80000
	s_addc_u32 s77, s43, 0
	s_add_i32 s38, s63, s47
	global_load_lds_dwordx4 v152, s[42:43]
	s_mov_b32 m0, s38
	s_nop 0
	global_load_lds_dwordx4 v148, s[76:77]
	s_add_i32 m0, s38, 0x2000
	s_nop 0
	global_load_lds_dwordx4 v152, s[76:77]
	s_mov_b32 m0, s50
	s_nop 0
	global_load_lds_dwordx4 v146, s[44:45]
	s_mov_b32 m0, s51
	s_nop 0
	global_load_lds_dwordx4 v150, s[44:45]
	s_waitcnt vmcnt(8)
	s_waitcnt lgkmcnt(0)
	s_barrier
	s_setprio 1
	s_waitcnt lgkmcnt(0)
	v_mfma_i32_16x16x64_i8 v[78:81], v[26:29], v[198:201], v[78:81]
	v_mfma_i32_16x16x64_i8 v[74:77], v[42:45], v[198:201], v[74:77]
	v_mfma_i32_16x16x64_i8 v[62:65], v[26:29], v[206:209], v[62:65]
	v_mfma_i32_16x16x64_i8 v[58:61], v[42:45], v[206:209], v[58:61]
	v_mfma_i32_16x16x64_i8 v[38:41], v[26:29], v[214:217], v[38:41]
	v_mfma_i32_16x16x64_i8 v[34:37], v[42:45], v[214:217], v[34:37]
	v_mfma_i32_16x16x64_i8 v[14:17], v[26:29], v[222:225], v[14:17]
	v_mfma_i32_16x16x64_i8 v[10:13], v[42:45], v[222:225], v[10:13]
	v_mfma_i32_16x16x64_i8 v[78:81], v[30:33], v[202:205], v[78:81]
	v_mfma_i32_16x16x64_i8 v[74:77], v[46:49], v[202:205], v[74:77]
	v_mfma_i32_16x16x64_i8 v[62:65], v[30:33], v[210:213], v[62:65]
	v_mfma_i32_16x16x64_i8 v[58:61], v[46:49], v[210:213], v[58:61]
	v_mfma_i32_16x16x64_i8 v[38:41], v[30:33], v[218:221], v[38:41]
	v_mfma_i32_16x16x64_i8 v[34:37], v[46:49], v[218:221], v[34:37]
	v_mfma_i32_16x16x64_i8 v[14:17], v[30:33], v[226:229], v[14:17]
	v_mfma_i32_16x16x64_i8 v[10:13], v[46:49], v[226:229], v[10:13]
	s_setprio 0
	s_setprio 1
	v_mfma_i32_16x16x64_i8 v[22:25], v[168:171], v[214:217], v[22:25]
	v_mfma_i32_16x16x64_i8 v[18:21], v[176:179], v[214:217], v[18:21]
	v_mfma_i32_16x16x64_i8 v[6:9], v[168:171], v[222:225], v[6:9]
	v_mfma_i32_16x16x64_i8 v[2:5], v[176:179], v[222:225], v[2:5]
	v_mfma_i32_16x16x64_i8 v[26:29], v[168:171], v[198:201], v[70:73]
	v_mfma_i32_16x16x64_i8 v[30:33], v[176:179], v[198:201], v[66:69]
	v_mfma_i32_16x16x64_i8 v[42:45], v[168:171], v[206:209], v[54:57]
	v_mfma_i32_16x16x64_i8 v[46:49], v[176:179], v[206:209], v[50:53]
	v_mfma_i32_16x16x64_i8 v[22:25], v[172:175], v[218:221], v[22:25]
	v_mfma_i32_16x16x64_i8 v[18:21], v[194:197], v[218:221], v[18:21]
	v_mfma_i32_16x16x64_i8 v[6:9], v[172:175], v[226:229], v[6:9]
	v_mfma_i32_16x16x64_i8 v[2:5], v[194:197], v[226:229], v[2:5]
	v_mfma_i32_16x16x64_i8 v[26:29], v[172:175], v[202:205], v[26:29]
	v_mfma_i32_16x16x64_i8 v[30:33], v[194:197], v[202:205], v[30:33]
	v_mfma_i32_16x16x64_i8 v[42:45], v[172:175], v[210:213], v[42:45]
	v_mfma_i32_16x16x64_i8 v[46:49], v[194:197], v[210:213], v[46:49]
	s_setprio 0
	s_barrier
	s_add_i32 s38, 0, 0x18000
	s_add_i32 s39, 0, 0x1c000
	v_add_u32_e32 v70, s38, v188
	v_add_u32_e32 v154, s39, v188
	ds_read_b128 v[50:53], v70
	ds_read_b128 v[54:57], v70 offset:1024
	ds_read_b128 v[66:69], v70 offset:2048
	ds_read_b128 v[70:73], v70 offset:3072
	ds_read_b128 v[168:171], v154
	ds_read_b128 v[172:175], v154 offset:1024
	ds_read_b128 v[176:179], v154 offset:2048
	ds_read_b128 v[194:197], v154 offset:3072
	s_add_u32 s44, s44, 0x80000
	s_addc_u32 s45, s45, 0
	s_mov_b32 m0, s52
	ds_read_b128 v[198:201], v193 offset:32768
	ds_read_b128 v[202:205], v193 offset:33792
	ds_read_b128 v[206:209], v193 offset:34816
	ds_read_b128 v[210:213], v193 offset:35840
	ds_read_b128 v[214:217], v193 offset:36864
	ds_read_b128 v[218:221], v193 offset:37888
	ds_read_b128 v[222:225], v193 offset:38912
	ds_read_b128 v[226:229], v193 offset:39936
	global_load_lds_dwordx4 v146, s[44:45]
	s_mov_b32 m0, s53
	s_nop 0
	global_load_lds_dwordx4 v150, s[44:45]
	s_waitcnt vmcnt(8)
	s_waitcnt lgkmcnt(0)
	s_barrier
	s_setprio 1
	s_waitcnt lgkmcnt(0)
	v_mfma_i32_16x16x64_i8 v[142:145], v[50:53], v[198:201], v[142:145]
	v_mfma_i32_16x16x64_i8 v[138:141], v[66:69], v[198:201], v[138:141]
	v_mfma_i32_16x16x64_i8 v[126:129], v[50:53], v[206:209], v[126:129]
	v_mfma_i32_16x16x64_i8 v[122:125], v[66:69], v[206:209], v[122:125]
	v_mfma_i32_16x16x64_i8 v[110:113], v[50:53], v[214:217], v[110:113]
	v_mfma_i32_16x16x64_i8 v[106:109], v[66:69], v[214:217], v[106:109]
	v_mfma_i32_16x16x64_i8 v[94:97], v[50:53], v[222:225], v[94:97]
	v_mfma_i32_16x16x64_i8 v[90:93], v[66:69], v[222:225], v[90:93]
	v_mfma_i32_16x16x64_i8 v[142:145], v[54:57], v[202:205], v[142:145]
	v_mfma_i32_16x16x64_i8 v[138:141], v[70:73], v[202:205], v[138:141]
	v_mfma_i32_16x16x64_i8 v[126:129], v[54:57], v[210:213], v[126:129]
	v_mfma_i32_16x16x64_i8 v[122:125], v[70:73], v[210:213], v[122:125]
	v_mfma_i32_16x16x64_i8 v[110:113], v[54:57], v[218:221], v[110:113]
	v_mfma_i32_16x16x64_i8 v[106:109], v[70:73], v[218:221], v[106:109]
	v_mfma_i32_16x16x64_i8 v[94:97], v[54:57], v[226:229], v[94:97]
	v_mfma_i32_16x16x64_i8 v[90:93], v[70:73], v[226:229], v[90:93]
	s_setprio 0
	s_setprio 1
	v_mfma_i32_16x16x64_i8 v[134:137], v[168:171], v[198:201], v[134:137]
	v_mfma_i32_16x16x64_i8 v[130:133], v[176:179], v[198:201], v[130:133]
	v_mfma_i32_16x16x64_i8 v[118:121], v[168:171], v[206:209], v[118:121]
	v_mfma_i32_16x16x64_i8 v[114:117], v[176:179], v[206:209], v[114:117]
	v_mfma_i32_16x16x64_i8 v[102:105], v[168:171], v[214:217], v[102:105]
	v_mfma_i32_16x16x64_i8 v[98:101], v[176:179], v[214:217], v[98:101]
	v_mfma_i32_16x16x64_i8 v[86:89], v[168:171], v[222:225], v[86:89]
	v_mfma_i32_16x16x64_i8 v[82:85], v[176:179], v[222:225], v[82:85]
	v_mfma_i32_16x16x64_i8 v[134:137], v[172:175], v[202:205], v[134:137]
	v_mfma_i32_16x16x64_i8 v[130:133], v[194:197], v[202:205], v[130:133]
	v_mfma_i32_16x16x64_i8 v[118:121], v[172:175], v[210:213], v[118:121]
	v_mfma_i32_16x16x64_i8 v[114:117], v[194:197], v[210:213], v[114:117]
	v_mfma_i32_16x16x64_i8 v[102:105], v[172:175], v[218:221], v[102:105]
	v_mfma_i32_16x16x64_i8 v[98:101], v[194:197], v[218:221], v[98:101]
	v_mfma_i32_16x16x64_i8 v[86:89], v[172:175], v[226:229], v[86:89]
	v_mfma_i32_16x16x64_i8 v[82:85], v[194:197], v[226:229], v[82:85]
	s_setprio 0
	s_barrier
	s_add_i32 s38, s38, s47
	s_mov_b32 m0, s38
	ds_read_b128 v[198:201], v193 offset:49152
	ds_read_b128 v[202:205], v193 offset:50176
	ds_read_b128 v[206:209], v193 offset:51200
	ds_read_b128 v[210:213], v193 offset:52224
	ds_read_b128 v[214:217], v193 offset:53248
	ds_read_b128 v[218:221], v193 offset:54272
	ds_read_b128 v[222:225], v193 offset:55296
	ds_read_b128 v[226:229], v193 offset:56320
	global_load_lds_dwordx4 v148, s[98:99]
	s_add_i32 m0, s38, 0x2000
	s_add_u32 s42, s42, 0x80080
	s_addc_u32 s43, s43, 0
	s_add_i32 s38, s39, s47
	global_load_lds_dwordx4 v152, s[98:99]
	s_mov_b32 m0, s38
	s_nop 0
	global_load_lds_dwordx4 v148, s[42:43]
	s_add_i32 m0, s38, 0x2000
	s_nop 0
	global_load_lds_dwordx4 v152, s[42:43]
	s_mov_b32 m0, s58
	s_nop 0
	global_load_lds_dwordx4 v146, s[100:101]
	s_mov_b32 m0, s59
	s_nop 0
	global_load_lds_dwordx4 v150, s[100:101]
	s_waitcnt vmcnt(8)
	s_waitcnt lgkmcnt(0)
	s_barrier
	s_setprio 1
	s_waitcnt lgkmcnt(0)
	v_mfma_i32_16x16x64_i8 v[78:81], v[50:53], v[198:201], v[78:81]
	v_mfma_i32_16x16x64_i8 v[74:77], v[66:69], v[198:201], v[74:77]
	v_mfma_i32_16x16x64_i8 v[62:65], v[50:53], v[206:209], v[62:65]
	v_mfma_i32_16x16x64_i8 v[58:61], v[66:69], v[206:209], v[58:61]
	v_mfma_i32_16x16x64_i8 v[38:41], v[50:53], v[214:217], v[38:41]
	v_mfma_i32_16x16x64_i8 v[34:37], v[66:69], v[214:217], v[34:37]
	v_mfma_i32_16x16x64_i8 v[14:17], v[50:53], v[222:225], v[14:17]
	v_mfma_i32_16x16x64_i8 v[10:13], v[66:69], v[222:225], v[10:13]
	v_mfma_i32_16x16x64_i8 v[78:81], v[54:57], v[202:205], v[78:81]
	v_mfma_i32_16x16x64_i8 v[74:77], v[70:73], v[202:205], v[74:77]
	v_mfma_i32_16x16x64_i8 v[62:65], v[54:57], v[210:213], v[62:65]
	v_mfma_i32_16x16x64_i8 v[58:61], v[70:73], v[210:213], v[58:61]
	v_mfma_i32_16x16x64_i8 v[38:41], v[54:57], v[218:221], v[38:41]
	v_mfma_i32_16x16x64_i8 v[34:37], v[70:73], v[218:221], v[34:37]
	v_mfma_i32_16x16x64_i8 v[14:17], v[54:57], v[226:229], v[14:17]
	v_mfma_i32_16x16x64_i8 v[10:13], v[70:73], v[226:229], v[10:13]
	s_setprio 0
	s_setprio 1
	v_mfma_i32_16x16x64_i8 v[26:29], v[168:171], v[198:201], v[26:29]
	v_mfma_i32_16x16x64_i8 v[70:73], v[172:175], v[202:205], v[26:29]
	v_mfma_i32_16x16x64_i8 v[26:29], v[176:179], v[198:201], v[30:33]
	v_mfma_i32_16x16x64_i8 v[66:69], v[194:197], v[202:205], v[26:29]
	v_mfma_i32_16x16x64_i8 v[26:29], v[168:171], v[206:209], v[42:45]
	v_mfma_i32_16x16x64_i8 v[54:57], v[172:175], v[210:213], v[26:29]
	v_mfma_i32_16x16x64_i8 v[26:29], v[176:179], v[206:209], v[46:49]
	v_mfma_i32_16x16x64_i8 v[22:25], v[168:171], v[214:217], v[22:25]
	v_mfma_i32_16x16x64_i8 v[18:21], v[176:179], v[214:217], v[18:21]
	v_mfma_i32_16x16x64_i8 v[6:9], v[168:171], v[222:225], v[6:9]
	v_mfma_i32_16x16x64_i8 v[2:5], v[176:179], v[222:225], v[2:5]
	v_mfma_i32_16x16x64_i8 v[50:53], v[194:197], v[210:213], v[26:29]
	v_mfma_i32_16x16x64_i8 v[22:25], v[172:175], v[218:221], v[22:25]
	v_mfma_i32_16x16x64_i8 v[18:21], v[194:197], v[218:221], v[18:21]
	v_mfma_i32_16x16x64_i8 v[6:9], v[172:175], v[226:229], v[6:9]
	v_mfma_i32_16x16x64_i8 v[2:5], v[194:197], v[226:229], v[2:5]
	s_setprio 0
	s_barrier
	s_add_i32 s74, s74, 2
	s_add_u32 s34, s34, 0x100
	s_addc_u32 s35, s35, 0
	s_add_u32 s67, s67, 0x100
	s_addc_u32 s73, s73, 0
	s_cmp_gt_u32 s74, 29
	s_cbranch_scc0 .LBB0_547
	s_and_b64 vcc, exec, s[14:15]
	s_cbranch_vccz .LBB0_550
	s_barrier

.LBB0_673:
	ds_read_b128 v[122:125], v167
	ds_read_b128 v[126:129], v167 offset:1024
	ds_read_b128 v[130:133], v167 offset:2048
	ds_read_b128 v[134:137], v167 offset:3072
	ds_read_b128 v[174:177], v171
	ds_read_b128 v[178:181], v171 offset:1024
	ds_read_b128 v[182:185], v171 offset:2048
	ds_read_b128 v[186:189], v171 offset:3072
	s_add_u32 s38, s44, 0xfff80080
	s_addc_u32 s39, s45, -1
	s_cmp_eq_u32 s77, 28
	s_cselect_b32 s47, s25, s39
	s_cselect_b32 s46, s73, s38
	s_cselect_b32 s43, s15, s76
	s_cselect_b32 s42, s74, s75
	s_add_i32 m0, s35, 0xc000
	ds_read_b128 v[190:193], v172
	ds_read_b128 v[194:197], v172 offset:1024
	ds_read_b128 v[198:201], v172 offset:2048
	ds_read_b128 v[202:205], v172 offset:3072
	ds_read_b128 v[206:209], v172 offset:4096
	ds_read_b128 v[210:213], v172 offset:5120
	ds_read_b128 v[214:217], v172 offset:6144
	ds_read_b128 v[218:221], v172 offset:7168
	global_load_lds_dwordx4 v156, s[44:45]
	s_add_i32 m0, s35, 0xe000
	s_nop 0
	global_load_lds_dwordx4 v158, s[44:45]
	s_waitcnt vmcnt(8)
	s_waitcnt lgkmcnt(0)
	s_barrier
	s_setprio 1
	s_waitcnt lgkmcnt(0)
	v_mfma_i32_16x16x64_i8 v[142:145], v[122:125], v[190:193], v[142:145]
	v_mfma_i32_16x16x64_i8 v[138:141], v[130:133], v[190:193], v[138:141]
	v_mfma_i32_16x16x64_i8 v[110:113], v[122:125], v[198:201], v[110:113]
	v_mfma_i32_16x16x64_i8 v[106:109], v[130:133], v[198:201], v[106:109]
	v_mfma_i32_16x16x64_i8 v[94:97], v[122:125], v[206:209], v[94:97]
	v_mfma_i32_16x16x64_i8 v[90:93], v[130:133], v[206:209], v[90:93]
	v_mfma_i32_16x16x64_i8 v[78:81], v[122:125], v[214:217], v[78:81]
	v_mfma_i32_16x16x64_i8 v[74:77], v[130:133], v[214:217], v[74:77]
	v_mfma_i32_16x16x64_i8 v[142:145], v[126:129], v[194:197], v[142:145]
	v_mfma_i32_16x16x64_i8 v[138:141], v[134:137], v[194:197], v[138:141]
	v_mfma_i32_16x16x64_i8 v[110:113], v[126:129], v[202:205], v[110:113]
	v_mfma_i32_16x16x64_i8 v[106:109], v[134:137], v[202:205], v[106:109]
	v_mfma_i32_16x16x64_i8 v[94:97], v[126:129], v[210:213], v[94:97]
	v_mfma_i32_16x16x64_i8 v[90:93], v[134:137], v[210:213], v[90:93]
	v_mfma_i32_16x16x64_i8 v[78:81], v[126:129], v[218:221], v[78:81]
	v_mfma_i32_16x16x64_i8 v[74:77], v[134:137], v[218:221], v[74:77]
	s_setprio 0
	s_setprio 1
	v_mfma_i32_16x16x64_i8 v[118:121], v[174:177], v[190:193], v[118:121]
	v_mfma_i32_16x16x64_i8 v[114:117], v[182:185], v[190:193], v[114:117]
	v_mfma_i32_16x16x64_i8 v[102:105], v[174:177], v[198:201], v[102:105]
	v_mfma_i32_16x16x64_i8 v[98:101], v[182:185], v[198:201], v[98:101]
	v_mfma_i32_16x16x64_i8 v[86:89], v[174:177], v[206:209], v[86:89]
	v_mfma_i32_16x16x64_i8 v[82:85], v[182:185], v[206:209], v[82:85]
	v_mfma_i32_16x16x64_i8 v[70:73], v[174:177], v[214:217], v[70:73]
	v_mfma_i32_16x16x64_i8 v[66:69], v[182:185], v[214:217], v[66:69]
	v_mfma_i32_16x16x64_i8 v[118:121], v[178:181], v[194:197], v[118:121]
	v_mfma_i32_16x16x64_i8 v[114:117], v[186:189], v[194:197], v[114:117]
	v_mfma_i32_16x16x64_i8 v[102:105], v[178:181], v[202:205], v[102:105]
	v_mfma_i32_16x16x64_i8 v[98:101], v[186:189], v[202:205], v[98:101]
	v_mfma_i32_16x16x64_i8 v[86:89], v[178:181], v[210:213], v[86:89]
	v_mfma_i32_16x16x64_i8 v[82:85], v[186:189], v[210:213], v[82:85]
	v_mfma_i32_16x16x64_i8 v[70:73], v[178:181], v[218:221], v[70:73]
	v_mfma_i32_16x16x64_i8 v[66:69], v[186:189], v[218:221], v[66:69]
	s_setprio 0
	s_barrier
	s_add_u32 s98, s42, s6
	s_addc_u32 s99, s43, s7
	s_add_u32 s100, s46, s6
	s_addc_u32 s101, s47, s7
	s_add_i32 s38, s66, s52
	s_mov_b32 m0, s38
	ds_read_b128 v[190:193], v172 offset:16384
	ds_read_b128 v[194:197], v172 offset:17408
	ds_read_b128 v[198:201], v172 offset:18432
	ds_read_b128 v[202:205], v172 offset:19456
	ds_read_b128 v[206:209], v172 offset:20480
	ds_read_b128 v[210:213], v172 offset:21504
	ds_read_b128 v[214:217], v172 offset:22528
	ds_read_b128 v[218:221], v172 offset:23552
	global_load_lds_dwordx4 v148, s[42:43]
	s_add_i32 m0, s38, 0x2000
	s_add_u32 s78, s42, 0x80000
	s_addc_u32 s79, s43, 0
	s_add_i32 s38, s67, s52
	global_load_lds_dwordx4 v152, s[42:43]
	s_mov_b32 m0, s38
	s_nop 0
	global_load_lds_dwordx4 v148, s[78:79]
	s_add_i32 m0, s38, 0x2000
	s_nop 0
	global_load_lds_dwordx4 v152, s[78:79]
	s_mov_b32 m0, s35
	s_nop 0
	global_load_lds_dwordx4 v146, s[46:47]
	s_mov_b32 m0, s53
	s_nop 0
	global_load_lds_dwordx4 v150, s[46:47]
	s_waitcnt vmcnt(8)
	s_waitcnt lgkmcnt(0)
	s_barrier
	s_setprio 1
	s_waitcnt lgkmcnt(0)
	v_mfma_i32_16x16x64_i8 v[62:65], v[122:125], v[190:193], v[62:65]
	v_mfma_i32_16x16x64_i8 v[58:61], v[130:133], v[190:193], v[58:61]
	v_mfma_i32_16x16x64_i8 v[46:49], v[122:125], v[198:201], v[46:49]
	v_mfma_i32_16x16x64_i8 v[42:45], v[130:133], v[198:201], v[42:45]
	v_mfma_i32_16x16x64_i8 v[30:33], v[122:125], v[206:209], v[30:33]
	v_mfma_i32_16x16x64_i8 v[26:29], v[130:133], v[206:209], v[26:29]
	v_mfma_i32_16x16x64_i8 v[14:17], v[122:125], v[214:217], v[14:17]
	v_mfma_i32_16x16x64_i8 v[10:13], v[130:133], v[214:217], v[10:13]
	v_mfma_i32_16x16x64_i8 v[62:65], v[126:129], v[194:197], v[62:65]
	v_mfma_i32_16x16x64_i8 v[58:61], v[134:137], v[194:197], v[58:61]
	v_mfma_i32_16x16x64_i8 v[46:49], v[126:129], v[202:205], v[46:49]
	v_mfma_i32_16x16x64_i8 v[42:45], v[134:137], v[202:205], v[42:45]
	v_mfma_i32_16x16x64_i8 v[30:33], v[126:129], v[210:213], v[30:33]
	v_mfma_i32_16x16x64_i8 v[26:29], v[134:137], v[210:213], v[26:29]
	v_mfma_i32_16x16x64_i8 v[14:17], v[126:129], v[218:221], v[14:17]
	v_mfma_i32_16x16x64_i8 v[10:13], v[134:137], v[218:221], v[10:13]
	s_setprio 0
	s_setprio 1
	v_mfma_i32_16x16x64_i8 v[54:57], v[174:177], v[190:193], v[54:57]
	v_mfma_i32_16x16x64_i8 v[50:53], v[182:185], v[190:193], v[50:53]
	v_mfma_i32_16x16x64_i8 v[38:41], v[174:177], v[198:201], v[38:41]
	v_mfma_i32_16x16x64_i8 v[34:37], v[182:185], v[198:201], v[34:37]
	v_mfma_i32_16x16x64_i8 v[22:25], v[174:177], v[206:209], v[22:25]
	v_mfma_i32_16x16x64_i8 v[18:21], v[182:185], v[206:209], v[18:21]
	v_mfma_i32_16x16x64_i8 v[6:9], v[174:177], v[214:217], v[6:9]
	v_mfma_i32_16x16x64_i8 v[2:5], v[182:185], v[214:217], v[2:5]
	v_mfma_i32_16x16x64_i8 v[54:57], v[178:181], v[194:197], v[54:57]
	v_mfma_i32_16x16x64_i8 v[50:53], v[186:189], v[194:197], v[50:53]
	v_mfma_i32_16x16x64_i8 v[38:41], v[178:181], v[202:205], v[38:41]
	v_mfma_i32_16x16x64_i8 v[34:37], v[186:189], v[202:205], v[34:37]
	v_mfma_i32_16x16x64_i8 v[22:25], v[178:181], v[210:213], v[22:25]
	v_mfma_i32_16x16x64_i8 v[18:21], v[186:189], v[210:213], v[18:21]
	v_mfma_i32_16x16x64_i8 v[6:9], v[178:181], v[218:221], v[6:9]
	v_mfma_i32_16x16x64_i8 v[2:5], v[186:189], v[218:221], v[2:5]
	s_setprio 0
	s_barrier
	s_add_i32 s38, 0, 0x18000
	s_add_i32 s39, 0, 0x1c000
	v_add_u32_e32 v134, s38, v169
	v_add_u32_e32 v154, s39, v169
	ds_read_b128 v[122:125], v134
	ds_read_b128 v[126:129], v134 offset:1024
	ds_read_b128 v[130:133], v134 offset:2048
	ds_read_b128 v[134:137], v134 offset:3072
	ds_read_b128 v[174:177], v154
	ds_read_b128 v[178:181], v154 offset:1024
	ds_read_b128 v[182:185], v154 offset:2048
	ds_read_b128 v[186:189], v154 offset:3072
	s_add_u32 s46, s46, 0x80000
	s_addc_u32 s47, s47, 0
	s_mov_b32 m0, s58
	ds_read_b128 v[190:193], v172 offset:32768
	ds_read_b128 v[194:197], v172 offset:33792
	ds_read_b128 v[198:201], v172 offset:34816
	ds_read_b128 v[202:205], v172 offset:35840
	ds_read_b128 v[206:209], v172 offset:36864
	ds_read_b128 v[210:213], v172 offset:37888
	ds_read_b128 v[214:217], v172 offset:38912
	ds_read_b128 v[218:221], v172 offset:39936
	global_load_lds_dwordx4 v146, s[46:47]
	s_mov_b32 m0, s59
	s_nop 0
	global_load_lds_dwordx4 v150, s[46:47]
	s_waitcnt vmcnt(8)
	s_waitcnt lgkmcnt(0)
	s_barrier
	s_setprio 1
	s_waitcnt lgkmcnt(0)
	v_mfma_i32_16x16x64_i8 v[142:145], v[122:125], v[190:193], v[142:145]
	v_mfma_i32_16x16x64_i8 v[138:141], v[130:133], v[190:193], v[138:141]
	v_mfma_i32_16x16x64_i8 v[110:113], v[122:125], v[198:201], v[110:113]
	v_mfma_i32_16x16x64_i8 v[106:109], v[130:133], v[198:201], v[106:109]
	v_mfma_i32_16x16x64_i8 v[94:97], v[122:125], v[206:209], v[94:97]
	v_mfma_i32_16x16x64_i8 v[90:93], v[130:133], v[206:209], v[90:93]
	v_mfma_i32_16x16x64_i8 v[78:81], v[122:125], v[214:217], v[78:81]
	v_mfma_i32_16x16x64_i8 v[74:77], v[130:133], v[214:217], v[74:77]
	v_mfma_i32_16x16x64_i8 v[142:145], v[126:129], v[194:197], v[142:145]
	v_mfma_i32_16x16x64_i8 v[138:141], v[134:137], v[194:197], v[138:141]
	v_mfma_i32_16x16x64_i8 v[110:113], v[126:129], v[202:205], v[110:113]
	v_mfma_i32_16x16x64_i8 v[106:109], v[134:137], v[202:205], v[106:109]
	v_mfma_i32_16x16x64_i8 v[94:97], v[126:129], v[210:213], v[94:97]
	v_mfma_i32_16x16x64_i8 v[90:93], v[134:137], v[210:213], v[90:93]
	v_mfma_i32_16x16x64_i8 v[78:81], v[126:129], v[218:221], v[78:81]
	v_mfma_i32_16x16x64_i8 v[74:77], v[134:137], v[218:221], v[74:77]
	s_setprio 0
	s_setprio 1
	v_mfma_i32_16x16x64_i8 v[118:121], v[174:177], v[190:193], v[118:121]
	v_mfma_i32_16x16x64_i8 v[114:117], v[182:185], v[190:193], v[114:117]
	v_mfma_i32_16x16x64_i8 v[102:105], v[174:177], v[198:201], v[102:105]
	v_mfma_i32_16x16x64_i8 v[98:101], v[182:185], v[198:201], v[98:101]
	v_mfma_i32_16x16x64_i8 v[86:89], v[174:177], v[206:209], v[86:89]
	v_mfma_i32_16x16x64_i8 v[82:85], v[182:185], v[206:209], v[82:85]
	v_mfma_i32_16x16x64_i8 v[70:73], v[174:177], v[214:217], v[70:73]
	v_mfma_i32_16x16x64_i8 v[66:69], v[182:185], v[214:217], v[66:69]
	v_mfma_i32_16x16x64_i8 v[118:121], v[178:181], v[194:197], v[118:121]
	v_mfma_i32_16x16x64_i8 v[114:117], v[186:189], v[194:197], v[114:117]
	v_mfma_i32_16x16x64_i8 v[102:105], v[178:181], v[202:205], v[102:105]
	v_mfma_i32_16x16x64_i8 v[98:101], v[186:189], v[202:205], v[98:101]
	v_mfma_i32_16x16x64_i8 v[86:89], v[178:181], v[210:213], v[86:89]
	v_mfma_i32_16x16x64_i8 v[82:85], v[186:189], v[210:213], v[82:85]
	v_mfma_i32_16x16x64_i8 v[70:73], v[178:181], v[218:221], v[70:73]
	v_mfma_i32_16x16x64_i8 v[66:69], v[186:189], v[218:221], v[66:69]
	s_setprio 0
	s_barrier
	s_add_i32 s38, s38, s52
	s_mov_b32 m0, s38
	ds_read_b128 v[190:193], v172 offset:49152
	ds_read_b128 v[194:197], v172 offset:50176
	ds_read_b128 v[198:201], v172 offset:51200
	ds_read_b128 v[202:205], v172 offset:52224
	ds_read_b128 v[206:209], v172 offset:53248
	ds_read_b128 v[210:213], v172 offset:54272
	ds_read_b128 v[214:217], v172 offset:55296
	ds_read_b128 v[218:221], v172 offset:56320
	global_load_lds_dwordx4 v148, s[98:99]
	s_add_i32 m0, s38, 0x2000
	s_add_u32 s42, s42, 0x80080
	s_addc_u32 s43, s43, 0
	s_add_i32 s38, s39, s52
	global_load_lds_dwordx4 v152, s[98:99]
	s_mov_b32 m0, s38
	s_nop 0
	global_load_lds_dwordx4 v148, s[42:43]
	s_add_i32 m0, s38, 0x2000
	s_nop 0
	global_load_lds_dwordx4 v152, s[42:43]
	s_mov_b32 m0, s61
	s_nop 0
	global_load_lds_dwordx4 v146, s[100:101]
	s_mov_b32 m0, s62
	s_nop 0
	global_load_lds_dwordx4 v150, s[100:101]
	s_waitcnt vmcnt(8)
	s_waitcnt lgkmcnt(0)
	s_barrier
	s_setprio 1
	s_waitcnt lgkmcnt(0)
	v_mfma_i32_16x16x64_i8 v[62:65], v[122:125], v[190:193], v[62:65]
	v_mfma_i32_16x16x64_i8 v[58:61], v[130:133], v[190:193], v[58:61]
	v_mfma_i32_16x16x64_i8 v[46:49], v[122:125], v[198:201], v[46:49]
	v_mfma_i32_16x16x64_i8 v[42:45], v[130:133], v[198:201], v[42:45]
	v_mfma_i32_16x16x64_i8 v[30:33], v[122:125], v[206:209], v[30:33]
	v_mfma_i32_16x16x64_i8 v[26:29], v[130:133], v[206:209], v[26:29]
	v_mfma_i32_16x16x64_i8 v[14:17], v[122:125], v[214:217], v[14:17]
	v_mfma_i32_16x16x64_i8 v[10:13], v[130:133], v[214:217], v[10:13]
	v_mfma_i32_16x16x64_i8 v[62:65], v[126:129], v[194:197], v[62:65]
	v_mfma_i32_16x16x64_i8 v[58:61], v[134:137], v[194:197], v[58:61]
	v_mfma_i32_16x16x64_i8 v[46:49], v[126:129], v[202:205], v[46:49]
	v_mfma_i32_16x16x64_i8 v[42:45], v[134:137], v[202:205], v[42:45]
	v_mfma_i32_16x16x64_i8 v[30:33], v[126:129], v[210:213], v[30:33]
	v_mfma_i32_16x16x64_i8 v[26:29], v[134:137], v[210:213], v[26:29]
	v_mfma_i32_16x16x64_i8 v[14:17], v[126:129], v[218:221], v[14:17]
	v_mfma_i32_16x16x64_i8 v[10:13], v[134:137], v[218:221], v[10:13]
	s_setprio 0
	s_setprio 1
	v_mfma_i32_16x16x64_i8 v[54:57], v[174:177], v[190:193], v[54:57]
	v_mfma_i32_16x16x64_i8 v[50:53], v[182:185], v[190:193], v[50:53]
	v_mfma_i32_16x16x64_i8 v[38:41], v[174:177], v[198:201], v[38:41]
	v_mfma_i32_16x16x64_i8 v[34:37], v[182:185], v[198:201], v[34:37]
	v_mfma_i32_16x16x64_i8 v[22:25], v[174:177], v[206:209], v[22:25]
	v_mfma_i32_16x16x64_i8 v[18:21], v[182:185], v[206:209], v[18:21]
	v_mfma_i32_16x16x64_i8 v[6:9], v[174:177], v[214:217], v[6:9]
	v_mfma_i32_16x16x64_i8 v[2:5], v[182:185], v[214:217], v[2:5]
	v_mfma_i32_16x16x64_i8 v[54:57], v[178:181], v[194:197], v[54:57]
	v_mfma_i32_16x16x64_i8 v[50:53], v[186:189], v[194:197], v[50:53]
	v_mfma_i32_16x16x64_i8 v[38:41], v[178:181], v[202:205], v[38:41]
	v_mfma_i32_16x16x64_i8 v[34:37], v[186:189], v[202:205], v[34:37]
	v_mfma_i32_16x16x64_i8 v[22:25], v[178:181], v[210:213], v[22:25]
	v_mfma_i32_16x16x64_i8 v[18:21], v[186:189], v[210:213], v[18:21]
	v_mfma_i32_16x16x64_i8 v[6:9], v[178:181], v[218:221], v[6:9]
	v_mfma_i32_16x16x64_i8 v[2:5], v[186:189], v[218:221], v[2:5]
	s_setprio 0
	s_barrier
	s_add_i32 s77, s77, 2
	s_add_u32 s44, s44, 0x100
	s_addc_u32 s45, s45, 0
	s_add_u32 s75, s75, 0x100
	s_addc_u32 s76, s76, 0
	s_cmp_gt_u32 s77, 29
	s_cbranch_scc0 .LBB0_673
	s_and_b64 vcc, exec, s[8:9]
	s_cbranch_vccz .LBB0_676
	s_barrier

.LBB0_1489:
	ds_read_b128 v[122:125], v169
	ds_read_b128 v[126:129], v169 offset:1024
	ds_read_b128 v[130:133], v169 offset:2048
	ds_read_b128 v[134:137], v169 offset:3072
	ds_read_b128 v[172:175], v170
	ds_read_b128 v[176:179], v170 offset:1024
	ds_read_b128 v[180:183], v170 offset:2048
	ds_read_b128 v[184:187], v170 offset:3072
	s_add_u32 s26, s24, 0xfff80080
	s_addc_u32 s27, s25, -1
	s_cmp_eq_u32 s53, 28
	s_cselect_b32 s29, s17, s27
	s_cselect_b32 s28, s49, s26
	s_cselect_b32 s27, s15, s52
	s_cselect_b32 s26, s50, s51
	s_add_i32 m0, s23, 0xc000
	ds_read_b128 v[188:191], v171
	ds_read_b128 v[192:195], v171 offset:1024
	ds_read_b128 v[196:199], v171 offset:2048
	ds_read_b128 v[200:203], v171 offset:3072
	ds_read_b128 v[204:207], v171 offset:4096
	ds_read_b128 v[208:211], v171 offset:5120
	ds_read_b128 v[212:215], v171 offset:6144
	ds_read_b128 v[216:219], v171 offset:7168
	global_load_lds_dwordx4 v156, s[24:25]
	s_add_i32 m0, s23, 0xe000
	s_nop 0
	global_load_lds_dwordx4 v158, s[24:25]
	s_waitcnt vmcnt(8)
	s_waitcnt lgkmcnt(0)
	s_barrier
	s_setprio 1
	s_waitcnt lgkmcnt(0)
	v_mfma_i32_16x16x64_i8 v[142:145], v[122:125], v[188:191], v[142:145]
	v_mfma_i32_16x16x64_i8 v[138:141], v[130:133], v[188:191], v[138:141]
	v_mfma_i32_16x16x64_i8 v[110:113], v[122:125], v[196:199], v[110:113]
	v_mfma_i32_16x16x64_i8 v[106:109], v[130:133], v[196:199], v[106:109]
	v_mfma_i32_16x16x64_i8 v[94:97], v[122:125], v[204:207], v[94:97]
	v_mfma_i32_16x16x64_i8 v[90:93], v[130:133], v[204:207], v[90:93]
	v_mfma_i32_16x16x64_i8 v[78:81], v[122:125], v[212:215], v[78:81]
	v_mfma_i32_16x16x64_i8 v[74:77], v[130:133], v[212:215], v[74:77]
	v_mfma_i32_16x16x64_i8 v[142:145], v[126:129], v[192:195], v[142:145]
	v_mfma_i32_16x16x64_i8 v[138:141], v[134:137], v[192:195], v[138:141]
	v_mfma_i32_16x16x64_i8 v[110:113], v[126:129], v[200:203], v[110:113]
	v_mfma_i32_16x16x64_i8 v[106:109], v[134:137], v[200:203], v[106:109]
	v_mfma_i32_16x16x64_i8 v[94:97], v[126:129], v[208:211], v[94:97]
	v_mfma_i32_16x16x64_i8 v[90:93], v[134:137], v[208:211], v[90:93]
	v_mfma_i32_16x16x64_i8 v[78:81], v[126:129], v[216:219], v[78:81]
	v_mfma_i32_16x16x64_i8 v[74:77], v[134:137], v[216:219], v[74:77]
	s_setprio 0
	s_setprio 1
	v_mfma_i32_16x16x64_i8 v[118:121], v[172:175], v[188:191], v[118:121]
	v_mfma_i32_16x16x64_i8 v[114:117], v[180:183], v[188:191], v[114:117]
	v_mfma_i32_16x16x64_i8 v[102:105], v[172:175], v[196:199], v[102:105]
	v_mfma_i32_16x16x64_i8 v[98:101], v[180:183], v[196:199], v[98:101]
	v_mfma_i32_16x16x64_i8 v[86:89], v[172:175], v[204:207], v[86:89]
	v_mfma_i32_16x16x64_i8 v[82:85], v[180:183], v[204:207], v[82:85]
	v_mfma_i32_16x16x64_i8 v[70:73], v[172:175], v[212:215], v[70:73]
	v_mfma_i32_16x16x64_i8 v[66:69], v[180:183], v[212:215], v[66:69]
	v_mfma_i32_16x16x64_i8 v[118:121], v[176:179], v[192:195], v[118:121]
	v_mfma_i32_16x16x64_i8 v[114:117], v[184:187], v[192:195], v[114:117]
	v_mfma_i32_16x16x64_i8 v[102:105], v[176:179], v[200:203], v[102:105]
	v_mfma_i32_16x16x64_i8 v[98:101], v[184:187], v[200:203], v[98:101]
	v_mfma_i32_16x16x64_i8 v[86:89], v[176:179], v[208:211], v[86:89]
	v_mfma_i32_16x16x64_i8 v[82:85], v[184:187], v[208:211], v[82:85]
	v_mfma_i32_16x16x64_i8 v[70:73], v[176:179], v[216:219], v[70:73]
	v_mfma_i32_16x16x64_i8 v[66:69], v[184:187], v[216:219], v[66:69]
	s_setprio 0
	s_barrier
	s_add_u32 s98, s26, s10
	s_addc_u32 s99, s27, s11
	s_add_u32 s100, s28, s10
	s_addc_u32 s101, s29, s11
	s_add_i32 s38, s46, s34
	s_mov_b32 m0, s38
	ds_read_b128 v[188:191], v171 offset:16384
	ds_read_b128 v[192:195], v171 offset:17408
	ds_read_b128 v[196:199], v171 offset:18432
	ds_read_b128 v[200:203], v171 offset:19456
	ds_read_b128 v[204:207], v171 offset:20480
	ds_read_b128 v[208:211], v171 offset:21504
	ds_read_b128 v[212:215], v171 offset:22528
	ds_read_b128 v[216:219], v171 offset:23552
	global_load_lds_dwordx4 v148, s[26:27]
	s_add_i32 m0, s38, 0x2000
	s_add_u32 s38, s26, 0x80000
	s_addc_u32 s39, s27, 0
	s_add_i32 s54, s47, s34
	global_load_lds_dwordx4 v152, s[26:27]
	s_mov_b32 m0, s54
	s_nop 0
	global_load_lds_dwordx4 v148, s[38:39]
	s_add_i32 m0, s54, 0x2000
	s_nop 0
	global_load_lds_dwordx4 v152, s[38:39]
	s_mov_b32 m0, s23
	s_nop 0
	global_load_lds_dwordx4 v146, s[28:29]
	s_mov_b32 m0, s35
	s_nop 0
	global_load_lds_dwordx4 v150, s[28:29]
	s_waitcnt vmcnt(8)
	s_waitcnt lgkmcnt(0)
	s_barrier
	s_setprio 1
	s_waitcnt lgkmcnt(0)
	v_mfma_i32_16x16x64_i8 v[62:65], v[122:125], v[188:191], v[62:65]
	v_mfma_i32_16x16x64_i8 v[58:61], v[130:133], v[188:191], v[58:61]
	v_mfma_i32_16x16x64_i8 v[46:49], v[122:125], v[196:199], v[46:49]
	v_mfma_i32_16x16x64_i8 v[42:45], v[130:133], v[196:199], v[42:45]
	v_mfma_i32_16x16x64_i8 v[30:33], v[122:125], v[204:207], v[30:33]
	v_mfma_i32_16x16x64_i8 v[26:29], v[130:133], v[204:207], v[26:29]
	v_mfma_i32_16x16x64_i8 v[14:17], v[122:125], v[212:215], v[14:17]
	v_mfma_i32_16x16x64_i8 v[10:13], v[130:133], v[212:215], v[10:13]
	v_mfma_i32_16x16x64_i8 v[62:65], v[126:129], v[192:195], v[62:65]
	v_mfma_i32_16x16x64_i8 v[58:61], v[134:137], v[192:195], v[58:61]
	v_mfma_i32_16x16x64_i8 v[46:49], v[126:129], v[200:203], v[46:49]
	v_mfma_i32_16x16x64_i8 v[42:45], v[134:137], v[200:203], v[42:45]
	v_mfma_i32_16x16x64_i8 v[30:33], v[126:129], v[208:211], v[30:33]
	v_mfma_i32_16x16x64_i8 v[26:29], v[134:137], v[208:211], v[26:29]
	v_mfma_i32_16x16x64_i8 v[14:17], v[126:129], v[216:219], v[14:17]
	v_mfma_i32_16x16x64_i8 v[10:13], v[134:137], v[216:219], v[10:13]
	s_setprio 0
	s_setprio 1
	v_mfma_i32_16x16x64_i8 v[54:57], v[172:175], v[188:191], v[54:57]
	v_mfma_i32_16x16x64_i8 v[50:53], v[180:183], v[188:191], v[50:53]
	v_mfma_i32_16x16x64_i8 v[38:41], v[172:175], v[196:199], v[38:41]
	v_mfma_i32_16x16x64_i8 v[34:37], v[180:183], v[196:199], v[34:37]
	v_mfma_i32_16x16x64_i8 v[22:25], v[172:175], v[204:207], v[22:25]
	v_mfma_i32_16x16x64_i8 v[18:21], v[180:183], v[204:207], v[18:21]
	v_mfma_i32_16x16x64_i8 v[6:9], v[172:175], v[212:215], v[6:9]
	v_mfma_i32_16x16x64_i8 v[2:5], v[180:183], v[212:215], v[2:5]
	v_mfma_i32_16x16x64_i8 v[54:57], v[176:179], v[192:195], v[54:57]
	v_mfma_i32_16x16x64_i8 v[50:53], v[184:187], v[192:195], v[50:53]
	v_mfma_i32_16x16x64_i8 v[38:41], v[176:179], v[200:203], v[38:41]
	v_mfma_i32_16x16x64_i8 v[34:37], v[184:187], v[200:203], v[34:37]
	v_mfma_i32_16x16x64_i8 v[22:25], v[176:179], v[208:211], v[22:25]
	v_mfma_i32_16x16x64_i8 v[18:21], v[184:187], v[208:211], v[18:21]
	v_mfma_i32_16x16x64_i8 v[6:9], v[176:179], v[216:219], v[6:9]
	v_mfma_i32_16x16x64_i8 v[2:5], v[184:187], v[216:219], v[2:5]
	s_setprio 0
	s_barrier
	s_add_i32 s38, 0, 0x18000
	s_add_i32 s39, 0, 0x1c000
	v_add_u32_e32 v134, s38, v167
	v_add_u32_e32 v154, s39, v167
	ds_read_b128 v[122:125], v134
	ds_read_b128 v[126:129], v134 offset:1024
	ds_read_b128 v[130:133], v134 offset:2048
	ds_read_b128 v[134:137], v134 offset:3072
	ds_read_b128 v[172:175], v154
	ds_read_b128 v[176:179], v154 offset:1024
	ds_read_b128 v[180:183], v154 offset:2048
	ds_read_b128 v[184:187], v154 offset:3072
	s_add_u32 s28, s28, 0x80000
	s_addc_u32 s29, s29, 0
	s_mov_b32 m0, s36
	ds_read_b128 v[188:191], v171 offset:32768
	ds_read_b128 v[192:195], v171 offset:33792
	ds_read_b128 v[196:199], v171 offset:34816
	ds_read_b128 v[200:203], v171 offset:35840
	ds_read_b128 v[204:207], v171 offset:36864
	ds_read_b128 v[208:211], v171 offset:37888
	ds_read_b128 v[212:215], v171 offset:38912
	ds_read_b128 v[216:219], v171 offset:39936
	global_load_lds_dwordx4 v146, s[28:29]
	s_mov_b32 m0, s37
	s_nop 0
	global_load_lds_dwordx4 v150, s[28:29]
	s_waitcnt vmcnt(8)
	s_waitcnt lgkmcnt(0)
	s_barrier
	s_setprio 1
	s_waitcnt lgkmcnt(0)
	v_mfma_i32_16x16x64_i8 v[142:145], v[122:125], v[188:191], v[142:145]
	v_mfma_i32_16x16x64_i8 v[138:141], v[130:133], v[188:191], v[138:141]
	v_mfma_i32_16x16x64_i8 v[110:113], v[122:125], v[196:199], v[110:113]
	v_mfma_i32_16x16x64_i8 v[106:109], v[130:133], v[196:199], v[106:109]
	v_mfma_i32_16x16x64_i8 v[94:97], v[122:125], v[204:207], v[94:97]
	v_mfma_i32_16x16x64_i8 v[90:93], v[130:133], v[204:207], v[90:93]
	v_mfma_i32_16x16x64_i8 v[78:81], v[122:125], v[212:215], v[78:81]
	v_mfma_i32_16x16x64_i8 v[74:77], v[130:133], v[212:215], v[74:77]
	v_mfma_i32_16x16x64_i8 v[142:145], v[126:129], v[192:195], v[142:145]
	v_mfma_i32_16x16x64_i8 v[138:141], v[134:137], v[192:195], v[138:141]
	v_mfma_i32_16x16x64_i8 v[110:113], v[126:129], v[200:203], v[110:113]
	v_mfma_i32_16x16x64_i8 v[106:109], v[134:137], v[200:203], v[106:109]
	v_mfma_i32_16x16x64_i8 v[94:97], v[126:129], v[208:211], v[94:97]
	v_mfma_i32_16x16x64_i8 v[90:93], v[134:137], v[208:211], v[90:93]
	v_mfma_i32_16x16x64_i8 v[78:81], v[126:129], v[216:219], v[78:81]
	v_mfma_i32_16x16x64_i8 v[74:77], v[134:137], v[216:219], v[74:77]
	s_setprio 0
	s_setprio 1
	v_mfma_i32_16x16x64_i8 v[118:121], v[172:175], v[188:191], v[118:121]
	v_mfma_i32_16x16x64_i8 v[114:117], v[180:183], v[188:191], v[114:117]
	v_mfma_i32_16x16x64_i8 v[102:105], v[172:175], v[196:199], v[102:105]
	v_mfma_i32_16x16x64_i8 v[98:101], v[180:183], v[196:199], v[98:101]
	v_mfma_i32_16x16x64_i8 v[86:89], v[172:175], v[204:207], v[86:89]
	v_mfma_i32_16x16x64_i8 v[82:85], v[180:183], v[204:207], v[82:85]
	v_mfma_i32_16x16x64_i8 v[70:73], v[172:175], v[212:215], v[70:73]
	v_mfma_i32_16x16x64_i8 v[66:69], v[180:183], v[212:215], v[66:69]
	v_mfma_i32_16x16x64_i8 v[118:121], v[176:179], v[192:195], v[118:121]
	v_mfma_i32_16x16x64_i8 v[114:117], v[184:187], v[192:195], v[114:117]
	v_mfma_i32_16x16x64_i8 v[102:105], v[176:179], v[200:203], v[102:105]
	v_mfma_i32_16x16x64_i8 v[98:101], v[184:187], v[200:203], v[98:101]
	v_mfma_i32_16x16x64_i8 v[86:89], v[176:179], v[208:211], v[86:89]
	v_mfma_i32_16x16x64_i8 v[82:85], v[184:187], v[208:211], v[82:85]
	v_mfma_i32_16x16x64_i8 v[70:73], v[176:179], v[216:219], v[70:73]
	v_mfma_i32_16x16x64_i8 v[66:69], v[184:187], v[216:219], v[66:69]
	s_setprio 0
	s_barrier
	s_add_i32 s28, s38, s34
	s_mov_b32 m0, s28
	ds_read_b128 v[188:191], v171 offset:49152
	ds_read_b128 v[192:195], v171 offset:50176
	ds_read_b128 v[196:199], v171 offset:51200
	ds_read_b128 v[200:203], v171 offset:52224
	ds_read_b128 v[204:207], v171 offset:53248
	ds_read_b128 v[208:211], v171 offset:54272
	ds_read_b128 v[212:215], v171 offset:55296
	ds_read_b128 v[216:219], v171 offset:56320
	global_load_lds_dwordx4 v148, s[98:99]
	s_add_i32 m0, s28, 0x2000
	s_add_u32 s26, s26, 0x80080
	s_addc_u32 s27, s27, 0
	s_add_i32 s28, s39, s34
	global_load_lds_dwordx4 v152, s[98:99]
	s_mov_b32 m0, s28
	s_nop 0
	global_load_lds_dwordx4 v148, s[26:27]
	s_add_i32 m0, s28, 0x2000
	s_nop 0
	global_load_lds_dwordx4 v152, s[26:27]
	s_mov_b32 m0, s43
	s_nop 0
	global_load_lds_dwordx4 v146, s[100:101]
	s_mov_b32 m0, s44
	s_nop 0
	global_load_lds_dwordx4 v150, s[100:101]
	s_waitcnt vmcnt(8)
	s_waitcnt lgkmcnt(0)
	s_barrier
	s_setprio 1
	s_waitcnt lgkmcnt(0)
	v_mfma_i32_16x16x64_i8 v[62:65], v[122:125], v[188:191], v[62:65]
	v_mfma_i32_16x16x64_i8 v[58:61], v[130:133], v[188:191], v[58:61]
	v_mfma_i32_16x16x64_i8 v[46:49], v[122:125], v[196:199], v[46:49]
	v_mfma_i32_16x16x64_i8 v[42:45], v[130:133], v[196:199], v[42:45]
	v_mfma_i32_16x16x64_i8 v[30:33], v[122:125], v[204:207], v[30:33]
	v_mfma_i32_16x16x64_i8 v[26:29], v[130:133], v[204:207], v[26:29]
	v_mfma_i32_16x16x64_i8 v[14:17], v[122:125], v[212:215], v[14:17]
	v_mfma_i32_16x16x64_i8 v[10:13], v[130:133], v[212:215], v[10:13]
	v_mfma_i32_16x16x64_i8 v[62:65], v[126:129], v[192:195], v[62:65]
	v_mfma_i32_16x16x64_i8 v[58:61], v[134:137], v[192:195], v[58:61]
	v_mfma_i32_16x16x64_i8 v[46:49], v[126:129], v[200:203], v[46:49]
	v_mfma_i32_16x16x64_i8 v[42:45], v[134:137], v[200:203], v[42:45]
	v_mfma_i32_16x16x64_i8 v[30:33], v[126:129], v[208:211], v[30:33]
	v_mfma_i32_16x16x64_i8 v[26:29], v[134:137], v[208:211], v[26:29]
	v_mfma_i32_16x16x64_i8 v[14:17], v[126:129], v[216:219], v[14:17]
	v_mfma_i32_16x16x64_i8 v[10:13], v[134:137], v[216:219], v[10:13]
	s_setprio 0
	s_setprio 1
	v_mfma_i32_16x16x64_i8 v[54:57], v[172:175], v[188:191], v[54:57]
	v_mfma_i32_16x16x64_i8 v[50:53], v[180:183], v[188:191], v[50:53]
	v_mfma_i32_16x16x64_i8 v[38:41], v[172:175], v[196:199], v[38:41]
	v_mfma_i32_16x16x64_i8 v[34:37], v[180:183], v[196:199], v[34:37]
	v_mfma_i32_16x16x64_i8 v[22:25], v[172:175], v[204:207], v[22:25]
	v_mfma_i32_16x16x64_i8 v[18:21], v[180:183], v[204:207], v[18:21]
	v_mfma_i32_16x16x64_i8 v[6:9], v[172:175], v[212:215], v[6:9]
	v_mfma_i32_16x16x64_i8 v[2:5], v[180:183], v[212:215], v[2:5]
	v_mfma_i32_16x16x64_i8 v[54:57], v[176:179], v[192:195], v[54:57]
	v_mfma_i32_16x16x64_i8 v[50:53], v[184:187], v[192:195], v[50:53]
	v_mfma_i32_16x16x64_i8 v[38:41], v[176:179], v[200:203], v[38:41]
	v_mfma_i32_16x16x64_i8 v[34:37], v[184:187], v[200:203], v[34:37]
	v_mfma_i32_16x16x64_i8 v[22:25], v[176:179], v[208:211], v[22:25]
	v_mfma_i32_16x16x64_i8 v[18:21], v[184:187], v[208:211], v[18:21]
	v_mfma_i32_16x16x64_i8 v[6:9], v[176:179], v[216:219], v[6:9]
	v_mfma_i32_16x16x64_i8 v[2:5], v[184:187], v[216:219], v[2:5]
	s_setprio 0
	s_barrier
	s_add_i32 s53, s53, 2
	s_add_u32 s24, s24, 0x100
	s_addc_u32 s25, s25, 0
	s_add_u32 s51, s51, 0x100
	s_addc_u32 s52, s52, 0
	s_cmp_gt_u32 s53, 29
	s_cbranch_scc0 .LBB0_1489
	s_and_b64 vcc, exec, s[12:13]
	s_cbranch_vccz .LBB0_1492
	s_barrier

.LBB0_1649:
	ds_read_b128 v[130:133], v167
	ds_read_b128 v[134:137], v167 offset:1024
	ds_read_b128 v[138:141], v167 offset:2048
	ds_read_b128 v[142:145], v167 offset:3072
	ds_read_b128 v[168:171], v228
	ds_read_b128 v[172:175], v228 offset:1024
	ds_read_b128 v[176:179], v228 offset:2048
	ds_read_b128 v[180:183], v228 offset:3072
	s_add_u32 s38, s34, 0xfff80080
	s_addc_u32 s39, s35, -1
	s_cmp_eq_u32 s77, 28
	s_cselect_b32 s45, s1, s39
	s_cselect_b32 s44, s29, s38
	s_cselect_b32 s43, s27, s47
	s_cselect_b32 s42, s41, s46
	s_add_i32 m0, s50, 0xc000
	ds_read_b128 v[184:187], v229
	ds_read_b128 v[188:191], v229 offset:1024
	ds_read_b128 v[192:195], v229 offset:2048
	ds_read_b128 v[196:199], v229 offset:3072
	ds_read_b128 v[200:203], v229 offset:4096
	ds_read_b128 v[204:207], v229 offset:5120
	ds_read_b128 v[208:211], v229 offset:6144
	ds_read_b128 v[212:215], v229 offset:7168
	global_load_lds_dwordx4 v158, s[34:35]
	s_add_i32 m0, s50, 0xe000
	s_nop 0
	global_load_lds_dwordx4 v160, s[34:35]
	s_waitcnt vmcnt(8)
	s_waitcnt lgkmcnt(0)
	s_barrier
	s_setprio 1
	s_waitcnt lgkmcnt(0)
	v_mfma_i32_16x16x64_i8 v[46:49], v[130:133], v[184:187], v[46:49]
	v_mfma_i32_16x16x64_i8 v[34:37], v[138:141], v[184:187], v[34:37]
	v_mfma_i32_16x16x64_i8 v[42:45], v[130:133], v[192:195], v[42:45]
	v_mfma_i32_16x16x64_i8 v[30:33], v[138:141], v[192:195], v[30:33]
	v_mfma_i32_16x16x64_i8 v[38:41], v[130:133], v[200:203], v[38:41]
	v_mfma_i32_16x16x64_i8 v[26:29], v[138:141], v[200:203], v[26:29]
	v_mfma_i32_16x16x64_i8 v[126:129], v[130:133], v[208:211], v[126:129]
	v_mfma_i32_16x16x64_i8 v[122:125], v[138:141], v[208:211], v[122:125]
	v_mfma_i32_16x16x64_i8 v[46:49], v[134:137], v[188:191], v[46:49]
	v_mfma_i32_16x16x64_i8 v[34:37], v[142:145], v[188:191], v[34:37]
	v_mfma_i32_16x16x64_i8 v[42:45], v[134:137], v[196:199], v[42:45]
	v_mfma_i32_16x16x64_i8 v[30:33], v[142:145], v[196:199], v[30:33]
	v_mfma_i32_16x16x64_i8 v[38:41], v[134:137], v[204:207], v[38:41]
	v_mfma_i32_16x16x64_i8 v[26:29], v[142:145], v[204:207], v[26:29]
	v_mfma_i32_16x16x64_i8 v[126:129], v[134:137], v[212:215], v[126:129]
	v_mfma_i32_16x16x64_i8 v[122:125], v[142:145], v[212:215], v[122:125]
	s_setprio 0
	s_setprio 1
	v_mfma_i32_16x16x64_i8 v[22:25], v[168:171], v[184:187], v[22:25]
	v_mfma_i32_16x16x64_i8 v[10:13], v[176:179], v[184:187], v[10:13]
	v_mfma_i32_16x16x64_i8 v[18:21], v[168:171], v[192:195], v[18:21]
	v_mfma_i32_16x16x64_i8 v[6:9], v[176:179], v[192:195], v[6:9]
	v_mfma_i32_16x16x64_i8 v[14:17], v[168:171], v[200:203], v[14:17]
	v_mfma_i32_16x16x64_i8 v[2:5], v[176:179], v[200:203], v[2:5]
	v_mfma_i32_16x16x64_i8 v[118:121], v[168:171], v[208:211], v[118:121]
	v_mfma_i32_16x16x64_i8 v[114:117], v[176:179], v[208:211], v[114:117]
	v_mfma_i32_16x16x64_i8 v[22:25], v[172:175], v[188:191], v[22:25]
	v_mfma_i32_16x16x64_i8 v[10:13], v[180:183], v[188:191], v[10:13]
	v_mfma_i32_16x16x64_i8 v[18:21], v[172:175], v[196:199], v[18:21]
	v_mfma_i32_16x16x64_i8 v[6:9], v[180:183], v[196:199], v[6:9]
	v_mfma_i32_16x16x64_i8 v[14:17], v[172:175], v[204:207], v[14:17]
	v_mfma_i32_16x16x64_i8 v[2:5], v[180:183], v[204:207], v[2:5]
	v_mfma_i32_16x16x64_i8 v[118:121], v[172:175], v[212:215], v[118:121]
	v_mfma_i32_16x16x64_i8 v[114:117], v[180:183], v[212:215], v[114:117]
	s_setprio 0
	s_barrier
	s_add_u32 s98, s42, s14
	s_addc_u32 s99, s43, s15
	s_add_u32 s100, s44, s14
	s_addc_u32 s101, s45, s15
	s_add_i32 s38, s64, s49
	s_mov_b32 m0, s38
	ds_read_b128 v[184:187], v229 offset:16384
	ds_read_b128 v[188:191], v229 offset:17408
	ds_read_b128 v[192:195], v229 offset:18432
	ds_read_b128 v[196:199], v229 offset:19456
	ds_read_b128 v[200:203], v229 offset:20480
	ds_read_b128 v[204:207], v229 offset:21504
	ds_read_b128 v[208:211], v229 offset:22528
	ds_read_b128 v[212:215], v229 offset:23552
	global_load_lds_dwordx4 v150, s[42:43]
	s_add_i32 m0, s38, 0x2000
	s_add_u32 s38, s42, 0x80000
	s_addc_u32 s39, s43, 0
	s_add_i32 s78, s65, s49
	global_load_lds_dwordx4 v154, s[42:43]
	s_mov_b32 m0, s78
	s_nop 0
	global_load_lds_dwordx4 v150, s[38:39]
	s_add_i32 m0, s78, 0x2000
	s_nop 0
	global_load_lds_dwordx4 v154, s[38:39]
	s_mov_b32 m0, s50
	s_nop 0
	global_load_lds_dwordx4 v148, s[44:45]
	s_mov_b32 m0, s51
	s_nop 0
	global_load_lds_dwordx4 v152, s[44:45]
	s_waitcnt vmcnt(8)
	s_waitcnt lgkmcnt(0)
	s_barrier
	s_setprio 1
	s_waitcnt lgkmcnt(0)
	v_mfma_i32_16x16x64_i8 v[94:97], v[130:133], v[184:187], v[94:97]
	v_mfma_i32_16x16x64_i8 v[70:73], v[138:141], v[184:187], v[70:73]
	v_mfma_i32_16x16x64_i8 v[86:89], v[130:133], v[192:195], v[86:89]
	v_mfma_i32_16x16x64_i8 v[62:65], v[138:141], v[192:195], v[62:65]
	v_mfma_i32_16x16x64_i8 v[78:81], v[130:133], v[200:203], v[78:81]
	v_mfma_i32_16x16x64_i8 v[54:57], v[138:141], v[200:203], v[54:57]
	v_mfma_i32_16x16x64_i8 v[110:113], v[130:133], v[208:211], v[110:113]
	v_mfma_i32_16x16x64_i8 v[106:109], v[138:141], v[208:211], v[106:109]
	v_mfma_i32_16x16x64_i8 v[94:97], v[134:137], v[188:191], v[94:97]
	v_mfma_i32_16x16x64_i8 v[70:73], v[142:145], v[188:191], v[70:73]
	v_mfma_i32_16x16x64_i8 v[86:89], v[134:137], v[196:199], v[86:89]
	v_mfma_i32_16x16x64_i8 v[62:65], v[142:145], v[196:199], v[62:65]
	v_mfma_i32_16x16x64_i8 v[78:81], v[134:137], v[204:207], v[78:81]
	v_mfma_i32_16x16x64_i8 v[54:57], v[142:145], v[204:207], v[54:57]
	v_mfma_i32_16x16x64_i8 v[110:113], v[134:137], v[212:215], v[110:113]
	v_mfma_i32_16x16x64_i8 v[106:109], v[142:145], v[212:215], v[106:109]
	s_setprio 0
	s_setprio 1
	v_mfma_i32_16x16x64_i8 v[90:93], v[168:171], v[184:187], v[90:93]
	v_mfma_i32_16x16x64_i8 v[66:69], v[176:179], v[184:187], v[66:69]
	v_mfma_i32_16x16x64_i8 v[82:85], v[168:171], v[192:195], v[82:85]
	v_mfma_i32_16x16x64_i8 v[58:61], v[176:179], v[192:195], v[58:61]
	v_mfma_i32_16x16x64_i8 v[74:77], v[168:171], v[200:203], v[74:77]
	v_mfma_i32_16x16x64_i8 v[50:53], v[176:179], v[200:203], v[50:53]
	v_mfma_i32_16x16x64_i8 v[102:105], v[168:171], v[208:211], v[102:105]
	v_mfma_i32_16x16x64_i8 v[98:101], v[176:179], v[208:211], v[98:101]
	v_mfma_i32_16x16x64_i8 v[90:93], v[172:175], v[188:191], v[90:93]
	v_mfma_i32_16x16x64_i8 v[66:69], v[180:183], v[188:191], v[66:69]
	v_mfma_i32_16x16x64_i8 v[82:85], v[172:175], v[196:199], v[82:85]
	v_mfma_i32_16x16x64_i8 v[58:61], v[180:183], v[196:199], v[58:61]
	v_mfma_i32_16x16x64_i8 v[74:77], v[172:175], v[204:207], v[74:77]
	v_mfma_i32_16x16x64_i8 v[50:53], v[180:183], v[204:207], v[50:53]
	v_mfma_i32_16x16x64_i8 v[102:105], v[172:175], v[212:215], v[102:105]
	v_mfma_i32_16x16x64_i8 v[98:101], v[180:183], v[212:215], v[98:101]
	s_setprio 0
	s_barrier
	s_add_i32 s78, 0, 0x18000
	s_add_i32 s79, 0, 0x1c000
	v_add_u32_e32 v142, s78, v1
	v_add_u32_e32 v156, s79, v1
	ds_read_b128 v[130:133], v142
	ds_read_b128 v[134:137], v142 offset:1024
	ds_read_b128 v[138:141], v142 offset:2048
	ds_read_b128 v[142:145], v142 offset:3072
	ds_read_b128 v[168:171], v156
	ds_read_b128 v[172:175], v156 offset:1024
	ds_read_b128 v[176:179], v156 offset:2048
	ds_read_b128 v[180:183], v156 offset:3072
	s_add_u32 s38, s44, 0x80000
	s_addc_u32 s39, s45, 0
	s_mov_b32 m0, s52
	ds_read_b128 v[184:187], v229 offset:32768
	ds_read_b128 v[188:191], v229 offset:33792
	ds_read_b128 v[192:195], v229 offset:34816
	ds_read_b128 v[196:199], v229 offset:35840
	ds_read_b128 v[200:203], v229 offset:36864
	ds_read_b128 v[204:207], v229 offset:37888
	ds_read_b128 v[208:211], v229 offset:38912
	ds_read_b128 v[212:215], v229 offset:39936
	global_load_lds_dwordx4 v148, s[38:39]
	s_mov_b32 m0, s53
	s_nop 0
	global_load_lds_dwordx4 v152, s[38:39]
	s_waitcnt vmcnt(8)
	s_waitcnt lgkmcnt(0)
	s_barrier
	s_setprio 1
	s_waitcnt lgkmcnt(0)
	v_mfma_i32_16x16x64_i8 v[46:49], v[130:133], v[184:187], v[46:49]
	v_mfma_i32_16x16x64_i8 v[34:37], v[138:141], v[184:187], v[34:37]
	v_mfma_i32_16x16x64_i8 v[42:45], v[130:133], v[192:195], v[42:45]
	v_mfma_i32_16x16x64_i8 v[30:33], v[138:141], v[192:195], v[30:33]
	v_mfma_i32_16x16x64_i8 v[38:41], v[130:133], v[200:203], v[38:41]
	v_mfma_i32_16x16x64_i8 v[26:29], v[138:141], v[200:203], v[26:29]
	v_mfma_i32_16x16x64_i8 v[126:129], v[130:133], v[208:211], v[126:129]
	v_mfma_i32_16x16x64_i8 v[122:125], v[138:141], v[208:211], v[122:125]
	v_mfma_i32_16x16x64_i8 v[46:49], v[134:137], v[188:191], v[46:49]
	v_mfma_i32_16x16x64_i8 v[34:37], v[142:145], v[188:191], v[34:37]
	v_mfma_i32_16x16x64_i8 v[42:45], v[134:137], v[196:199], v[42:45]
	v_mfma_i32_16x16x64_i8 v[30:33], v[142:145], v[196:199], v[30:33]
	v_mfma_i32_16x16x64_i8 v[38:41], v[134:137], v[204:207], v[38:41]
	v_mfma_i32_16x16x64_i8 v[26:29], v[142:145], v[204:207], v[26:29]
	v_mfma_i32_16x16x64_i8 v[126:129], v[134:137], v[212:215], v[126:129]
	v_mfma_i32_16x16x64_i8 v[122:125], v[142:145], v[212:215], v[122:125]
	s_setprio 0
	s_setprio 1
	v_mfma_i32_16x16x64_i8 v[22:25], v[168:171], v[184:187], v[22:25]
	v_mfma_i32_16x16x64_i8 v[10:13], v[176:179], v[184:187], v[10:13]
	v_mfma_i32_16x16x64_i8 v[18:21], v[168:171], v[192:195], v[18:21]
	v_mfma_i32_16x16x64_i8 v[6:9], v[176:179], v[192:195], v[6:9]
	v_mfma_i32_16x16x64_i8 v[14:17], v[168:171], v[200:203], v[14:17]
	v_mfma_i32_16x16x64_i8 v[2:5], v[176:179], v[200:203], v[2:5]
	v_mfma_i32_16x16x64_i8 v[118:121], v[168:171], v[208:211], v[118:121]
	v_mfma_i32_16x16x64_i8 v[114:117], v[176:179], v[208:211], v[114:117]
	v_mfma_i32_16x16x64_i8 v[22:25], v[172:175], v[188:191], v[22:25]
	v_mfma_i32_16x16x64_i8 v[10:13], v[180:183], v[188:191], v[10:13]
	v_mfma_i32_16x16x64_i8 v[18:21], v[172:175], v[196:199], v[18:21]
	v_mfma_i32_16x16x64_i8 v[6:9], v[180:183], v[196:199], v[6:9]
	v_mfma_i32_16x16x64_i8 v[14:17], v[172:175], v[204:207], v[14:17]
	v_mfma_i32_16x16x64_i8 v[2:5], v[180:183], v[204:207], v[2:5]
	v_mfma_i32_16x16x64_i8 v[118:121], v[172:175], v[212:215], v[118:121]
	v_mfma_i32_16x16x64_i8 v[114:117], v[180:183], v[212:215], v[114:117]
	s_setprio 0
	s_barrier
	s_add_i32 s38, s78, s49
	s_mov_b32 m0, s38
	ds_read_b128 v[184:187], v229 offset:49152
	ds_read_b128 v[188:191], v229 offset:50176
	ds_read_b128 v[192:195], v229 offset:51200
	ds_read_b128 v[196:199], v229 offset:52224
	ds_read_b128 v[200:203], v229 offset:53248
	ds_read_b128 v[204:207], v229 offset:54272
	ds_read_b128 v[208:211], v229 offset:55296
	ds_read_b128 v[212:215], v229 offset:56320
	global_load_lds_dwordx4 v150, s[98:99]
	s_add_i32 m0, s38, 0x2000
	s_add_u32 s38, s42, 0x80080
	s_addc_u32 s39, s43, 0
	s_add_i32 s42, s79, s49
	global_load_lds_dwordx4 v154, s[98:99]
	s_mov_b32 m0, s42
	s_nop 0
	global_load_lds_dwordx4 v150, s[38:39]
	s_add_i32 m0, s42, 0x2000
	s_nop 0
	global_load_lds_dwordx4 v154, s[38:39]
	s_mov_b32 m0, s57
	s_nop 0
	global_load_lds_dwordx4 v148, s[100:101]
	s_mov_b32 m0, s58
	s_nop 0
	global_load_lds_dwordx4 v152, s[100:101]
	s_waitcnt vmcnt(8)
	s_waitcnt lgkmcnt(0)
	s_barrier
	s_setprio 1
	s_waitcnt lgkmcnt(0)
	v_mfma_i32_16x16x64_i8 v[94:97], v[130:133], v[184:187], v[94:97]
	v_mfma_i32_16x16x64_i8 v[70:73], v[138:141], v[184:187], v[70:73]
	v_mfma_i32_16x16x64_i8 v[86:89], v[130:133], v[192:195], v[86:89]
	v_mfma_i32_16x16x64_i8 v[62:65], v[138:141], v[192:195], v[62:65]
	v_mfma_i32_16x16x64_i8 v[78:81], v[130:133], v[200:203], v[78:81]
	v_mfma_i32_16x16x64_i8 v[54:57], v[138:141], v[200:203], v[54:57]
	v_mfma_i32_16x16x64_i8 v[110:113], v[130:133], v[208:211], v[110:113]
	v_mfma_i32_16x16x64_i8 v[106:109], v[138:141], v[208:211], v[106:109]
	v_mfma_i32_16x16x64_i8 v[94:97], v[134:137], v[188:191], v[94:97]
	v_mfma_i32_16x16x64_i8 v[70:73], v[142:145], v[188:191], v[70:73]
	v_mfma_i32_16x16x64_i8 v[86:89], v[134:137], v[196:199], v[86:89]
	v_mfma_i32_16x16x64_i8 v[62:65], v[142:145], v[196:199], v[62:65]
	v_mfma_i32_16x16x64_i8 v[78:81], v[134:137], v[204:207], v[78:81]
	v_mfma_i32_16x16x64_i8 v[54:57], v[142:145], v[204:207], v[54:57]
	v_mfma_i32_16x16x64_i8 v[110:113], v[134:137], v[212:215], v[110:113]
	v_mfma_i32_16x16x64_i8 v[106:109], v[142:145], v[212:215], v[106:109]
	s_setprio 0
	s_setprio 1
	v_mfma_i32_16x16x64_i8 v[90:93], v[168:171], v[184:187], v[90:93]
	v_mfma_i32_16x16x64_i8 v[66:69], v[176:179], v[184:187], v[66:69]
	v_mfma_i32_16x16x64_i8 v[82:85], v[168:171], v[192:195], v[82:85]
	v_mfma_i32_16x16x64_i8 v[58:61], v[176:179], v[192:195], v[58:61]
	v_mfma_i32_16x16x64_i8 v[74:77], v[168:171], v[200:203], v[74:77]
	v_mfma_i32_16x16x64_i8 v[50:53], v[176:179], v[200:203], v[50:53]
	v_mfma_i32_16x16x64_i8 v[102:105], v[168:171], v[208:211], v[102:105]
	v_mfma_i32_16x16x64_i8 v[98:101], v[176:179], v[208:211], v[98:101]
	v_mfma_i32_16x16x64_i8 v[90:93], v[172:175], v[188:191], v[90:93]
	v_mfma_i32_16x16x64_i8 v[66:69], v[180:183], v[188:191], v[66:69]
	v_mfma_i32_16x16x64_i8 v[82:85], v[172:175], v[196:199], v[82:85]
	v_mfma_i32_16x16x64_i8 v[58:61], v[180:183], v[196:199], v[58:61]
	v_mfma_i32_16x16x64_i8 v[74:77], v[172:175], v[204:207], v[74:77]
	v_mfma_i32_16x16x64_i8 v[50:53], v[180:183], v[204:207], v[50:53]
	v_mfma_i32_16x16x64_i8 v[102:105], v[172:175], v[212:215], v[102:105]
	v_mfma_i32_16x16x64_i8 v[98:101], v[180:183], v[212:215], v[98:101]
	s_setprio 0
	s_barrier
	s_add_i32 s77, s77, 2
	s_add_u32 s34, s34, 0x100
	s_addc_u32 s35, s35, 0
	s_add_u32 s46, s46, 0x100
	s_addc_u32 s47, s47, 0
	s_cmp_gt_u32 s77, 29
	s_cbranch_scc0 .LBB0_1649
	s_and_b64 vcc, exec, s[16:17]
	s_cbranch_vccz .LBB0_1652
	s_barrier

.LBB0_1899:
	ds_read_b128 v[122:125], v169
	ds_read_b128 v[126:129], v169 offset:1024
	ds_read_b128 v[130:133], v169 offset:2048
	ds_read_b128 v[134:137], v169 offset:3072
	ds_read_b128 v[172:175], v170
	ds_read_b128 v[176:179], v170 offset:1024
	ds_read_b128 v[180:183], v170 offset:2048
	ds_read_b128 v[184:187], v170 offset:3072
	s_add_u32 s22, s20, 0xffea8080
	s_addc_u32 s23, s21, -1
	s_cmpk_eq_i32 s49, 0x52
	s_cselect_b32 s25, s5, s23
	s_cselect_b32 s24, s4, s22
	s_cselect_b32 s23, s19, s48
	s_cselect_b32 s22, s18, s47
	s_add_i32 m0, s30, 0xc000
	ds_read_b128 v[188:191], v171
	ds_read_b128 v[192:195], v171 offset:1024
	ds_read_b128 v[196:199], v171 offset:2048
	ds_read_b128 v[200:203], v171 offset:3072
	ds_read_b128 v[204:207], v171 offset:4096
	ds_read_b128 v[208:211], v171 offset:5120
	ds_read_b128 v[212:215], v171 offset:6144
	ds_read_b128 v[216:219], v171 offset:7168
	global_load_lds_dwordx4 v156, s[20:21]
	s_add_i32 m0, s30, 0xe000
	s_nop 0
	global_load_lds_dwordx4 v158, s[20:21]
	s_waitcnt vmcnt(8)
	s_waitcnt lgkmcnt(0)
	s_barrier
	s_setprio 1
	s_waitcnt lgkmcnt(0)
	v_mfma_i32_16x16x64_i8 v[142:145], v[122:125], v[188:191], v[142:145]
	v_mfma_i32_16x16x64_i8 v[138:141], v[130:133], v[188:191], v[138:141]
	v_mfma_i32_16x16x64_i8 v[110:113], v[122:125], v[196:199], v[110:113]
	v_mfma_i32_16x16x64_i8 v[106:109], v[130:133], v[196:199], v[106:109]
	v_mfma_i32_16x16x64_i8 v[94:97], v[122:125], v[204:207], v[94:97]
	v_mfma_i32_16x16x64_i8 v[90:93], v[130:133], v[204:207], v[90:93]
	v_mfma_i32_16x16x64_i8 v[78:81], v[122:125], v[212:215], v[78:81]
	v_mfma_i32_16x16x64_i8 v[74:77], v[130:133], v[212:215], v[74:77]
	v_mfma_i32_16x16x64_i8 v[142:145], v[126:129], v[192:195], v[142:145]
	v_mfma_i32_16x16x64_i8 v[138:141], v[134:137], v[192:195], v[138:141]
	v_mfma_i32_16x16x64_i8 v[110:113], v[126:129], v[200:203], v[110:113]
	v_mfma_i32_16x16x64_i8 v[106:109], v[134:137], v[200:203], v[106:109]
	v_mfma_i32_16x16x64_i8 v[94:97], v[126:129], v[208:211], v[94:97]
	v_mfma_i32_16x16x64_i8 v[90:93], v[134:137], v[208:211], v[90:93]
	v_mfma_i32_16x16x64_i8 v[78:81], v[126:129], v[216:219], v[78:81]
	v_mfma_i32_16x16x64_i8 v[74:77], v[134:137], v[216:219], v[74:77]
	s_setprio 0
	s_setprio 1
	v_mfma_i32_16x16x64_i8 v[118:121], v[172:175], v[188:191], v[118:121]
	v_mfma_i32_16x16x64_i8 v[114:117], v[180:183], v[188:191], v[114:117]
	v_mfma_i32_16x16x64_i8 v[102:105], v[172:175], v[196:199], v[102:105]
	v_mfma_i32_16x16x64_i8 v[98:101], v[180:183], v[196:199], v[98:101]
	v_mfma_i32_16x16x64_i8 v[86:89], v[172:175], v[204:207], v[86:89]
	v_mfma_i32_16x16x64_i8 v[82:85], v[180:183], v[204:207], v[82:85]
	v_mfma_i32_16x16x64_i8 v[70:73], v[172:175], v[212:215], v[70:73]
	v_mfma_i32_16x16x64_i8 v[66:69], v[180:183], v[212:215], v[66:69]
	v_mfma_i32_16x16x64_i8 v[118:121], v[176:179], v[192:195], v[118:121]
	v_mfma_i32_16x16x64_i8 v[114:117], v[184:187], v[192:195], v[114:117]
	v_mfma_i32_16x16x64_i8 v[102:105], v[176:179], v[200:203], v[102:105]
	v_mfma_i32_16x16x64_i8 v[98:101], v[184:187], v[200:203], v[98:101]
	v_mfma_i32_16x16x64_i8 v[86:89], v[176:179], v[208:211], v[86:89]
	v_mfma_i32_16x16x64_i8 v[82:85], v[184:187], v[208:211], v[82:85]
	v_mfma_i32_16x16x64_i8 v[70:73], v[176:179], v[216:219], v[70:73]
	v_mfma_i32_16x16x64_i8 v[66:69], v[184:187], v[216:219], v[66:69]
	s_setprio 0
	s_barrier
	s_add_u32 s98, s22, s14
	s_addc_u32 s99, s23, s15
	s_add_u32 s100, s24, s14
	s_addc_u32 s101, s25, s15
	s_add_i32 s38, s41, s29
	s_mov_b32 m0, s38
	ds_read_b128 v[188:191], v171 offset:16384
	ds_read_b128 v[192:195], v171 offset:17408
	ds_read_b128 v[196:199], v171 offset:18432
	ds_read_b128 v[200:203], v171 offset:19456
	ds_read_b128 v[204:207], v171 offset:20480
	ds_read_b128 v[208:211], v171 offset:21504
	ds_read_b128 v[212:215], v171 offset:22528
	ds_read_b128 v[216:219], v171 offset:23552
	global_load_lds_dwordx4 v148, s[22:23]
	s_add_i32 m0, s38, 0x2000
	s_add_u32 s38, s22, 0x158000
	s_addc_u32 s39, s23, 0
	s_add_i32 s50, s42, s29
	global_load_lds_dwordx4 v152, s[22:23]
	s_mov_b32 m0, s50
	s_nop 0
	global_load_lds_dwordx4 v148, s[38:39]
	s_add_i32 m0, s50, 0x2000
	s_nop 0
	global_load_lds_dwordx4 v152, s[38:39]
	s_mov_b32 m0, s30
	s_nop 0
	global_load_lds_dwordx4 v146, s[24:25]
	s_mov_b32 m0, s31
	s_nop 0
	global_load_lds_dwordx4 v150, s[24:25]
	s_waitcnt vmcnt(8)
	s_waitcnt lgkmcnt(0)
	s_barrier
	s_setprio 1
	s_waitcnt lgkmcnt(0)
	v_mfma_i32_16x16x64_i8 v[62:65], v[122:125], v[188:191], v[62:65]
	v_mfma_i32_16x16x64_i8 v[58:61], v[130:133], v[188:191], v[58:61]
	v_mfma_i32_16x16x64_i8 v[46:49], v[122:125], v[196:199], v[46:49]
	v_mfma_i32_16x16x64_i8 v[42:45], v[130:133], v[196:199], v[42:45]
	v_mfma_i32_16x16x64_i8 v[30:33], v[122:125], v[204:207], v[30:33]
	v_mfma_i32_16x16x64_i8 v[26:29], v[130:133], v[204:207], v[26:29]
	v_mfma_i32_16x16x64_i8 v[14:17], v[122:125], v[212:215], v[14:17]
	v_mfma_i32_16x16x64_i8 v[10:13], v[130:133], v[212:215], v[10:13]
	v_mfma_i32_16x16x64_i8 v[62:65], v[126:129], v[192:195], v[62:65]
	v_mfma_i32_16x16x64_i8 v[58:61], v[134:137], v[192:195], v[58:61]
	v_mfma_i32_16x16x64_i8 v[46:49], v[126:129], v[200:203], v[46:49]
	v_mfma_i32_16x16x64_i8 v[42:45], v[134:137], v[200:203], v[42:45]
	v_mfma_i32_16x16x64_i8 v[30:33], v[126:129], v[208:211], v[30:33]
	v_mfma_i32_16x16x64_i8 v[26:29], v[134:137], v[208:211], v[26:29]
	v_mfma_i32_16x16x64_i8 v[14:17], v[126:129], v[216:219], v[14:17]
	v_mfma_i32_16x16x64_i8 v[10:13], v[134:137], v[216:219], v[10:13]
	s_setprio 0
	s_setprio 1
	v_mfma_i32_16x16x64_i8 v[54:57], v[172:175], v[188:191], v[54:57]
	v_mfma_i32_16x16x64_i8 v[50:53], v[180:183], v[188:191], v[50:53]
	v_mfma_i32_16x16x64_i8 v[38:41], v[172:175], v[196:199], v[38:41]
	v_mfma_i32_16x16x64_i8 v[34:37], v[180:183], v[196:199], v[34:37]
	v_mfma_i32_16x16x64_i8 v[22:25], v[172:175], v[204:207], v[22:25]
	v_mfma_i32_16x16x64_i8 v[18:21], v[180:183], v[204:207], v[18:21]
	v_mfma_i32_16x16x64_i8 v[6:9], v[172:175], v[212:215], v[6:9]
	v_mfma_i32_16x16x64_i8 v[2:5], v[180:183], v[212:215], v[2:5]
	v_mfma_i32_16x16x64_i8 v[54:57], v[176:179], v[192:195], v[54:57]
	v_mfma_i32_16x16x64_i8 v[50:53], v[184:187], v[192:195], v[50:53]
	v_mfma_i32_16x16x64_i8 v[38:41], v[176:179], v[200:203], v[38:41]
	v_mfma_i32_16x16x64_i8 v[34:37], v[184:187], v[200:203], v[34:37]
	v_mfma_i32_16x16x64_i8 v[22:25], v[176:179], v[208:211], v[22:25]
	v_mfma_i32_16x16x64_i8 v[18:21], v[184:187], v[208:211], v[18:21]
	v_mfma_i32_16x16x64_i8 v[6:9], v[176:179], v[216:219], v[6:9]
	v_mfma_i32_16x16x64_i8 v[2:5], v[184:187], v[216:219], v[2:5]
	s_setprio 0
	s_barrier
	s_add_i32 s38, 0, 0x18000
	s_add_i32 s39, 0, 0x1c000
	v_add_u32_e32 v134, s38, v167
	v_add_u32_e32 v154, s39, v167
	ds_read_b128 v[122:125], v134
	ds_read_b128 v[126:129], v134 offset:1024
	ds_read_b128 v[130:133], v134 offset:2048
	ds_read_b128 v[134:137], v134 offset:3072
	ds_read_b128 v[172:175], v154
	ds_read_b128 v[176:179], v154 offset:1024
	ds_read_b128 v[180:183], v154 offset:2048
	ds_read_b128 v[184:187], v154 offset:3072
	s_add_u32 s24, s24, 0x158000
	s_addc_u32 s25, s25, 0
	s_mov_b32 m0, s33
	ds_read_b128 v[188:191], v171 offset:32768
	ds_read_b128 v[192:195], v171 offset:33792
	ds_read_b128 v[196:199], v171 offset:34816
	ds_read_b128 v[200:203], v171 offset:35840
	ds_read_b128 v[204:207], v171 offset:36864
	ds_read_b128 v[208:211], v171 offset:37888
	ds_read_b128 v[212:215], v171 offset:38912
	ds_read_b128 v[216:219], v171 offset:39936
	global_load_lds_dwordx4 v146, s[24:25]
	s_mov_b32 m0, s34
	s_nop 0
	global_load_lds_dwordx4 v150, s[24:25]
	s_waitcnt vmcnt(8)
	s_waitcnt lgkmcnt(0)
	s_barrier
	s_setprio 1
	s_waitcnt lgkmcnt(0)
	v_mfma_i32_16x16x64_i8 v[142:145], v[122:125], v[188:191], v[142:145]
	v_mfma_i32_16x16x64_i8 v[138:141], v[130:133], v[188:191], v[138:141]
	v_mfma_i32_16x16x64_i8 v[110:113], v[122:125], v[196:199], v[110:113]
	v_mfma_i32_16x16x64_i8 v[106:109], v[130:133], v[196:199], v[106:109]
	v_mfma_i32_16x16x64_i8 v[94:97], v[122:125], v[204:207], v[94:97]
	v_mfma_i32_16x16x64_i8 v[90:93], v[130:133], v[204:207], v[90:93]
	v_mfma_i32_16x16x64_i8 v[78:81], v[122:125], v[212:215], v[78:81]
	v_mfma_i32_16x16x64_i8 v[74:77], v[130:133], v[212:215], v[74:77]
	v_mfma_i32_16x16x64_i8 v[142:145], v[126:129], v[192:195], v[142:145]
	v_mfma_i32_16x16x64_i8 v[138:141], v[134:137], v[192:195], v[138:141]
	v_mfma_i32_16x16x64_i8 v[110:113], v[126:129], v[200:203], v[110:113]
	v_mfma_i32_16x16x64_i8 v[106:109], v[134:137], v[200:203], v[106:109]
	v_mfma_i32_16x16x64_i8 v[94:97], v[126:129], v[208:211], v[94:97]
	v_mfma_i32_16x16x64_i8 v[90:93], v[134:137], v[208:211], v[90:93]
	v_mfma_i32_16x16x64_i8 v[78:81], v[126:129], v[216:219], v[78:81]
	v_mfma_i32_16x16x64_i8 v[74:77], v[134:137], v[216:219], v[74:77]
	s_setprio 0
	s_setprio 1
	v_mfma_i32_16x16x64_i8 v[118:121], v[172:175], v[188:191], v[118:121]
	v_mfma_i32_16x16x64_i8 v[114:117], v[180:183], v[188:191], v[114:117]
	v_mfma_i32_16x16x64_i8 v[102:105], v[172:175], v[196:199], v[102:105]
	v_mfma_i32_16x16x64_i8 v[98:101], v[180:183], v[196:199], v[98:101]
	v_mfma_i32_16x16x64_i8 v[86:89], v[172:175], v[204:207], v[86:89]
	v_mfma_i32_16x16x64_i8 v[82:85], v[180:183], v[204:207], v[82:85]
	v_mfma_i32_16x16x64_i8 v[70:73], v[172:175], v[212:215], v[70:73]
	v_mfma_i32_16x16x64_i8 v[66:69], v[180:183], v[212:215], v[66:69]
	v_mfma_i32_16x16x64_i8 v[118:121], v[176:179], v[192:195], v[118:121]
	v_mfma_i32_16x16x64_i8 v[114:117], v[184:187], v[192:195], v[114:117]
	v_mfma_i32_16x16x64_i8 v[102:105], v[176:179], v[200:203], v[102:105]
	v_mfma_i32_16x16x64_i8 v[98:101], v[184:187], v[200:203], v[98:101]
	v_mfma_i32_16x16x64_i8 v[86:89], v[176:179], v[208:211], v[86:89]
	v_mfma_i32_16x16x64_i8 v[82:85], v[184:187], v[208:211], v[82:85]
	v_mfma_i32_16x16x64_i8 v[70:73], v[176:179], v[216:219], v[70:73]
	v_mfma_i32_16x16x64_i8 v[66:69], v[184:187], v[216:219], v[66:69]
	s_setprio 0
	s_barrier
	s_add_i32 s24, s38, s29
	s_mov_b32 m0, s24
	ds_read_b128 v[188:191], v171 offset:49152
	ds_read_b128 v[192:195], v171 offset:50176
	ds_read_b128 v[196:199], v171 offset:51200
	ds_read_b128 v[200:203], v171 offset:52224
	ds_read_b128 v[204:207], v171 offset:53248
	ds_read_b128 v[208:211], v171 offset:54272
	ds_read_b128 v[212:215], v171 offset:55296
	ds_read_b128 v[216:219], v171 offset:56320
	global_load_lds_dwordx4 v148, s[98:99]
	s_add_i32 m0, s24, 0x2000
	s_add_u32 s22, s22, 0x158080
	s_addc_u32 s23, s23, 0
	s_add_i32 s24, s39, s29
	global_load_lds_dwordx4 v152, s[98:99]
	s_mov_b32 m0, s24
	s_nop 0
	global_load_lds_dwordx4 v148, s[22:23]
	s_add_i32 m0, s24, 0x2000
	s_nop 0
	global_load_lds_dwordx4 v152, s[22:23]
	s_mov_b32 m0, s36
	s_nop 0
	global_load_lds_dwordx4 v146, s[100:101]
	s_mov_b32 m0, s37
	s_nop 0
	global_load_lds_dwordx4 v150, s[100:101]
	s_waitcnt vmcnt(8)
	s_waitcnt lgkmcnt(0)
	s_barrier
	s_setprio 1
	s_waitcnt lgkmcnt(0)
	v_mfma_i32_16x16x64_i8 v[62:65], v[122:125], v[188:191], v[62:65]
	v_mfma_i32_16x16x64_i8 v[58:61], v[130:133], v[188:191], v[58:61]
	v_mfma_i32_16x16x64_i8 v[46:49], v[122:125], v[196:199], v[46:49]
	v_mfma_i32_16x16x64_i8 v[42:45], v[130:133], v[196:199], v[42:45]
	v_mfma_i32_16x16x64_i8 v[30:33], v[122:125], v[204:207], v[30:33]
	v_mfma_i32_16x16x64_i8 v[26:29], v[130:133], v[204:207], v[26:29]
	v_mfma_i32_16x16x64_i8 v[14:17], v[122:125], v[212:215], v[14:17]
	v_mfma_i32_16x16x64_i8 v[10:13], v[130:133], v[212:215], v[10:13]
	v_mfma_i32_16x16x64_i8 v[62:65], v[126:129], v[192:195], v[62:65]
	v_mfma_i32_16x16x64_i8 v[58:61], v[134:137], v[192:195], v[58:61]
	v_mfma_i32_16x16x64_i8 v[46:49], v[126:129], v[200:203], v[46:49]
	v_mfma_i32_16x16x64_i8 v[42:45], v[134:137], v[200:203], v[42:45]
	v_mfma_i32_16x16x64_i8 v[30:33], v[126:129], v[208:211], v[30:33]
	v_mfma_i32_16x16x64_i8 v[26:29], v[134:137], v[208:211], v[26:29]
	v_mfma_i32_16x16x64_i8 v[14:17], v[126:129], v[216:219], v[14:17]
	v_mfma_i32_16x16x64_i8 v[10:13], v[134:137], v[216:219], v[10:13]
	s_setprio 0
	s_setprio 1
	v_mfma_i32_16x16x64_i8 v[54:57], v[172:175], v[188:191], v[54:57]
	v_mfma_i32_16x16x64_i8 v[50:53], v[180:183], v[188:191], v[50:53]
	v_mfma_i32_16x16x64_i8 v[38:41], v[172:175], v[196:199], v[38:41]
	v_mfma_i32_16x16x64_i8 v[34:37], v[180:183], v[196:199], v[34:37]
	v_mfma_i32_16x16x64_i8 v[22:25], v[172:175], v[204:207], v[22:25]
	v_mfma_i32_16x16x64_i8 v[18:21], v[180:183], v[204:207], v[18:21]
	v_mfma_i32_16x16x64_i8 v[6:9], v[172:175], v[212:215], v[6:9]
	v_mfma_i32_16x16x64_i8 v[2:5], v[180:183], v[212:215], v[2:5]
	v_mfma_i32_16x16x64_i8 v[54:57], v[176:179], v[192:195], v[54:57]
	v_mfma_i32_16x16x64_i8 v[50:53], v[184:187], v[192:195], v[50:53]
	v_mfma_i32_16x16x64_i8 v[38:41], v[176:179], v[200:203], v[38:41]
	v_mfma_i32_16x16x64_i8 v[34:37], v[184:187], v[200:203], v[34:37]
	v_mfma_i32_16x16x64_i8 v[22:25], v[176:179], v[208:211], v[22:25]
	v_mfma_i32_16x16x64_i8 v[18:21], v[184:187], v[208:211], v[18:21]
	v_mfma_i32_16x16x64_i8 v[6:9], v[176:179], v[216:219], v[6:9]
	v_mfma_i32_16x16x64_i8 v[2:5], v[184:187], v[216:219], v[2:5]
	s_setprio 0
	s_barrier
	s_add_i32 s49, s49, 2
	s_add_u32 s20, s20, 0x100
	s_addc_u32 s21, s21, 0
	s_add_u32 s47, s47, 0x100
	s_addc_u32 s48, s48, 0
	s_cmpk_gt_u32 s49, 0x53
	s_cbranch_scc0 .LBB0_1899
	s_and_b64 vcc, exec, s[16:17]
	s_cbranch_vccz .LBB0_1902
	s_barrier
